# c14
# speedup vs baseline: 1.0158x; 1.0020x over previous
.LBB6_32:
	s_or_b64 exec, exec, s[12:13]
	s_lshl_b32 s62, s59, 10
	v_add_lshl_u32 v2, v1, s62, 10
	v_lshl_add_u32 v2, v185, 15, v2
	v_or_b32_e32 v166, v2, v206
	v_mov_b32_e32 v154, 0
	v_mov_b32_e32 v50, 0
	v_mov_b32_e32 v14, 0
	v_mov_b32_e32 v15, 0
	v_mov_b32_e32 v16, 0
	v_mov_b32_e32 v17, 0
	s_and_saveexec_b64 s[12:13], s[34:35]
	s_cbranch_execz .LBB6_34
	v_mov_b32_e32 v3, 0
	v_or_b32_e32 v2, 0x200, v166
	v_mov_b32_e32 v167, v3
	v_lshl_add_u64 v[4:5], v[2:3], 4, s[20:21]
	v_lshl_add_u64 v[2:3], v[166:167], 2, s[22:23]
	global_load_dwordx4 v[14:17], v[4:5], off
	global_load_dword v50, v[2:3], off offset:2048

.LBB6_40:
	s_or_b64 exec, exec, s[12:13]
	v_and_b32_e32 v198, 2, v194
	v_lshlrev_b32_e32 v19, 2, v194
	v_lshl_add_u32 v18, v186, 1, v198
	v_and_b32_e32 v197, 4, v19
	v_mad_u32_u24 v18, v18, 10, v197
	v_mul_u32_u24_e32 v22, 0x420, v18
	v_add_lshl_u32 v18, v190, v206, 4
	v_add3_u32 v195, v22, v18, 0
	s_waitcnt lgkmcnt(0)
	s_barrier
	ds_read_b128 v[18:21], v195
	v_mov_b32_e32 v23, 0x220
	s_waitcnt vmcnt(23) lgkmcnt(0)
	v_mfma_f32_32x32x16_f16 v[30:45], v[150:153], v[18:21], 0
	v_cmp_gt_u32_e64 s[12:13], 32, v182
	s_nop 1
	v_cndmask_b32_e64 v23, v23, 32, s[12:13]
	v_add_u32_e32 v18, v23, v55
	v_add3_u32 v196, v18, v22, 0
	ds_read_b128 v[18:21], v196
	ds_read_b128 v[22:25], v195 offset:1056
	ds_read_b128 v[26:29], v195 offset:2112
	ds_read_b128 v[46:49], v196 offset:1056
	ds_read_b128 v[156:159], v196 offset:2112
	s_waitcnt vmcnt(22) lgkmcnt(4)
	v_mfma_f32_32x32x16_f16 v[30:45], v[146:149], v[18:21], v[30:45]
	s_waitcnt vmcnt(21) lgkmcnt(3)
	v_mfma_f32_32x32x16_f16 v[30:45], v[142:145], v[22:25], v[30:45]
	ds_read_b128 v[18:21], v195 offset:3168
	ds_read_b128 v[22:25], v196 offset:3168
	s_waitcnt vmcnt(20) lgkmcnt(3)
	v_mfma_f32_32x32x16_f16 v[30:45], v[134:137], v[46:49], v[30:45]
	s_waitcnt vmcnt(19)
	v_mfma_f32_32x32x16_f16 v[30:45], v[138:141], v[26:29], v[30:45]
	ds_read_b128 v[26:29], v195 offset:4224
	ds_read_b128 v[46:49], v196 offset:4224
	s_waitcnt vmcnt(18) lgkmcnt(4)
	v_mfma_f32_32x32x16_f16 v[30:45], v[130:133], v[156:159], v[30:45]
	s_waitcnt vmcnt(17) lgkmcnt(3)
	v_mfma_f32_32x32x16_f16 v[30:45], v[126:129], v[18:21], v[30:45]
	ds_read_b128 v[18:21], v195 offset:5280
	ds_read_b128 v[156:159], v196 offset:5280
	s_waitcnt vmcnt(16) lgkmcnt(4)
	v_mfma_f32_32x32x16_f16 v[30:45], v[118:121], v[22:25], v[30:45]
	s_waitcnt vmcnt(15) lgkmcnt(3)
	v_mfma_f32_32x32x16_f16 v[30:45], v[122:125], v[26:29], v[30:45]
	ds_read_b128 v[22:25], v195 offset:10560
	ds_read_b128 v[160:163], v196 offset:10560
	s_waitcnt vmcnt(14) lgkmcnt(4)
	v_mfma_f32_32x32x16_f16 v[30:45], v[110:113], v[46:49], v[30:45]
	s_waitcnt vmcnt(13) lgkmcnt(3)
	v_mfma_f32_32x32x16_f16 v[30:45], v[114:117], v[18:21], v[30:45]
	ds_read_b128 v[46:49], v195 offset:11616
	ds_read_b128 v[174:177], v196 offset:11616
	s_waitcnt vmcnt(12) lgkmcnt(4)
	v_mfma_f32_32x32x16_f16 v[30:45], v[102:105], v[156:159], v[30:45]
	s_waitcnt vmcnt(11) lgkmcnt(3)
	v_mfma_f32_32x32x16_f16 v[30:45], v[106:109], v[22:25], v[30:45]
	ds_read_b128 v[26:29], v195 offset:12672
	ds_read_b128 v[18:21], v196 offset:12672
	s_waitcnt vmcnt(10) lgkmcnt(4)
	v_mfma_f32_32x32x16_f16 v[30:45], v[98:101], v[160:163], v[30:45]
	s_waitcnt vmcnt(9) lgkmcnt(3)
	v_mfma_f32_32x32x16_f16 v[30:45], v[94:97], v[46:49], v[30:45]
	ds_read_b128 v[46:49], v195 offset:13728
	ds_read_b128 v[22:25], v196 offset:13728
	s_mov_b64 s[12:13], s[40:41]
	s_waitcnt vmcnt(1)
	ds_write_b128 v192, v[14:17] offset:63376
	s_waitcnt vmcnt(0)
	ds_write_b32 v192, v50 offset:63908
	s_waitcnt lgkmcnt(6)
	v_mfma_f32_32x32x16_f16 v[30:45], v[86:89], v[174:177], v[30:45]
	s_and_saveexec_b64 s[14:15], s[8:9]
	s_andn2_b64 s[12:13], s[40:41], exec
	s_and_b64 s[44:45], s[10:11], exec
	s_or_b64 s[12:13], s[12:13], s[44:45]
	ds_write_b32 v192, v50 offset:63896
	s_or_b64 exec, exec, s[14:15]
	s_and_saveexec_b64 s[14:15], s[12:13]
	ds_write_b32 v192, v50 offset:63920
	s_or_b64 exec, exec, s[14:15]
	s_waitcnt lgkmcnt(5)
	v_mfma_f32_32x32x16_f16 v[30:45], v[90:93], v[26:29], v[30:45]
	ds_read_b128 v[50:53], v195 offset:14784
	ds_read_b128 v[26:29], v196 offset:14784
	s_waitcnt lgkmcnt(6)
	v_mfma_f32_32x32x16_f16 v[30:45], v[82:85], v[18:21], v[30:45]
	s_waitcnt lgkmcnt(5)
	v_mfma_f32_32x32x16_f16 v[30:45], v[78:81], v[46:49], v[30:45]
	ds_read_b128 v[18:21], v195 offset:15840
	ds_read_b128 v[14:17], v196 offset:15840
	s_mov_b64 s[12:13], s[40:41]
	ds_write_b128 v193, v[10:13] offset:63376
	ds_write_b32 v193, v154 offset:63908
	s_waitcnt lgkmcnt(8)
	v_mfma_f32_32x32x16_f16 v[30:45], v[58:61], v[22:25], v[30:45]
	s_and_saveexec_b64 s[14:15], s[8:9]
	s_andn2_b64 s[12:13], s[40:41], exec
	s_and_b64 s[44:45], s[10:11], exec
	s_or_b64 s[12:13], s[12:13], s[44:45]
	ds_write_b32 v193, v154 offset:63896
	s_or_b64 exec, exec, s[14:15]
	s_and_saveexec_b64 s[14:15], s[12:13]
	ds_write_b32 v193, v154 offset:63920
	s_or_b64 exec, exec, s[14:15]
	s_movk_i32 s12, 0x420
	v_mad_u32_u24 v10, v54, s12, 0
	s_waitcnt lgkmcnt(5)
	v_mfma_f32_32x32x16_f16 v[30:45], v[70:73], v[50:53], v[30:45]
	v_add_u32_e32 v200, v10, v55
	s_waitcnt lgkmcnt(4)
	v_mfma_f32_32x32x16_f16 v[30:45], v[62:65], v[26:29], v[30:45]
	s_and_saveexec_b64 s[12:13], s[4:5]
	s_cbranch_execz .LBB6_53
	s_mov_b64 s[44:45], s[40:41]
	ds_write_b128 v200, v[6:9] offset:63376
	ds_write_b32 v200, v155 offset:63908
	s_and_saveexec_b64 s[14:15], s[8:9]
	s_andn2_b64 s[44:45], s[40:41], exec
	s_and_b64 s[46:47], s[10:11], exec
	s_or_b64 s[44:45], s[44:45], s[46:47]
	ds_write_b32 v200, v155 offset:63896
	s_or_b64 exec, exec, s[14:15]
	s_and_b64 exec, exec, s[44:45]
	ds_write_b32 v200, v155 offset:63920

.LBB6_58:
	s_or_b64 exec, exec, s[12:13]
	v_mov_b32_e32 v159, 0
	v_mov_b32_e32 v161, 0
	v_mov_b32_e32 v14, 0
	v_mov_b32_e32 v15, 0
	v_mov_b32_e32 v16, 0
	v_mov_b32_e32 v17, 0
	s_and_saveexec_b64 s[12:13], s[34:35]
	s_cbranch_execz .LBB6_60
	v_mov_b32_e32 v3, 0
	v_or_b32_e32 v2, 0x220, v166
	v_mov_b32_e32 v167, v3
	v_lshl_add_u64 v[4:5], v[2:3], 4, s[20:21]
	v_lshl_add_u64 v[2:3], v[166:167], 2, s[22:23]
	global_load_dwordx4 v[14:17], v[4:5], off
	global_load_dword v161, v[2:3], off offset:2176

.LBB6_66:
	s_or_b64 exec, exec, s[12:13]
	s_waitcnt lgkmcnt(0)
	s_barrier
	ds_read_b128 v[18:21], v195 offset:63360
	ds_read_b128 v[22:25], v196 offset:63360
	v_add_u32_e32 v202, 0xf780, v195
	v_add_u32_e32 v203, 0xf780, v196
	s_waitcnt lgkmcnt(1)
	v_mfma_f32_32x32x16_f16 v[42:57], v[150:153], v[18:21], 0
	ds_read_b128 v[18:21], v195 offset:64416
	ds_read_b128 v[26:29], v195 offset:65472
	ds_read_b128 v[154:157], v196 offset:64416
	ds_read_b128 v[162:165], v196 offset:65472
	s_waitcnt lgkmcnt(4)
	v_mfma_f32_32x32x16_f16 v[42:57], v[146:149], v[22:25], v[42:57]
	s_waitcnt lgkmcnt(3)
	v_mfma_f32_32x32x16_f16 v[42:57], v[142:145], v[18:21], v[42:57]
	ds_read_b128 v[18:21], v202 offset:3168
	ds_read_b128 v[22:25], v203 offset:3168
	s_waitcnt lgkmcnt(3)
	v_mfma_f32_32x32x16_f16 v[42:57], v[134:137], v[154:157], v[42:57]
	v_mfma_f32_32x32x16_f16 v[42:57], v[138:141], v[26:29], v[42:57]
	ds_read_b128 v[26:29], v202 offset:4224
	ds_read_b128 v[154:157], v203 offset:4224
	s_waitcnt lgkmcnt(4)
	v_mfma_f32_32x32x16_f16 v[42:57], v[130:133], v[162:165], v[42:57]
	s_waitcnt lgkmcnt(3)
	v_mfma_f32_32x32x16_f16 v[42:57], v[126:129], v[18:21], v[42:57]
	ds_read_b128 v[18:21], v202 offset:5280
	ds_read_b128 v[162:165], v203 offset:5280
	s_waitcnt lgkmcnt(4)
	v_mfma_f32_32x32x16_f16 v[42:57], v[118:121], v[22:25], v[42:57]
	s_waitcnt lgkmcnt(3)
	v_mfma_f32_32x32x16_f16 v[42:57], v[122:125], v[26:29], v[42:57]
	ds_read_b128 v[22:25], v202 offset:10560
	ds_read_b128 v[174:177], v203 offset:10560
	s_waitcnt lgkmcnt(4)
	v_mfma_f32_32x32x16_f16 v[42:57], v[110:113], v[154:157], v[42:57]
	s_waitcnt lgkmcnt(3)
	v_mfma_f32_32x32x16_f16 v[42:57], v[114:117], v[18:21], v[42:57]
	ds_read_b128 v[18:21], v202 offset:11616
	ds_read_b128 v[210:213], v203 offset:11616
	s_waitcnt lgkmcnt(4)
	v_mfma_f32_32x32x16_f16 v[42:57], v[102:105], v[162:165], v[42:57]
	s_waitcnt lgkmcnt(3)
	v_mfma_f32_32x32x16_f16 v[42:57], v[106:109], v[22:25], v[42:57]
	ds_read_b128 v[26:29], v202 offset:12672
	ds_read_b128 v[154:157], v203 offset:12672
	s_waitcnt lgkmcnt(4)
	v_mfma_f32_32x32x16_f16 v[42:57], v[98:101], v[174:177], v[42:57]
	s_waitcnt lgkmcnt(3)
	v_mfma_f32_32x32x16_f16 v[42:57], v[94:97], v[18:21], v[42:57]
	ds_read_b128 v[22:25], v202 offset:13728
	ds_read_b128 v[18:21], v203 offset:13728
	s_mov_b64 s[12:13], s[40:41]
	s_waitcnt vmcnt(1)
	ds_write_b128 v192, v[14:17] offset:16
	s_waitcnt vmcnt(0)
	ds_write_b32 v192, v161 offset:548
	s_waitcnt lgkmcnt(6)
	v_mfma_f32_32x32x16_f16 v[42:57], v[86:89], v[210:213], v[42:57]
	s_and_saveexec_b64 s[14:15], s[8:9]
	s_andn2_b64 s[12:13], s[40:41], exec
	s_and_b64 s[44:45], s[10:11], exec
	s_or_b64 s[12:13], s[12:13], s[44:45]
	ds_write_b32 v192, v161 offset:536
	s_or_b64 exec, exec, s[14:15]
	s_and_saveexec_b64 s[14:15], s[12:13]
	ds_write_b32 v192, v161 offset:560
	s_or_b64 exec, exec, s[14:15]
	v_lshlrev_b32_e32 v14, 11, v194
	s_add_i32 s44, 0, 0x1ef00
	v_lshlrev_b32_e32 v15, 2, v182
	v_cmp_eq_u32_e64 s[12:13], 0, v186
	v_cmp_ne_u32_e64 s[14:15], 0, v186
	v_add3_u32 v199, s44, v14, v15
	s_waitcnt lgkmcnt(5)
	v_mfma_f32_32x32x16_f16 v[42:57], v[90:93], v[26:29], v[42:57]
	ds_read_b128 v[26:29], v202 offset:14784
	ds_read_b128 v[14:17], v203 offset:14784
	s_waitcnt lgkmcnt(6)
	v_mfma_f32_32x32x16_f16 v[42:57], v[82:85], v[154:157], v[42:57]
	s_and_saveexec_b64 s[44:45], s[14:15]
	s_xor_b64 s[44:45], exec, s[44:45]
	v_add_f32_e32 v38, 0, v38
	v_add_f32_e32 v39, 0, v39
	ds_write2st64_b32 v199, v38, v39 offset1:1
	s_andn2_saveexec_b64 s[44:45], s[44:45]
	s_or_b64 exec, exec, s[44:45]
	s_and_saveexec_b64 s[44:45], s[14:15]
	s_xor_b64 s[44:45], exec, s[44:45]
	v_add_f32_e32 v38, 0, v40
	v_add_f32_e32 v39, 0, v41
	ds_write2st64_b32 v199, v38, v39 offset0:2 offset1:3
	s_andn2_saveexec_b64 s[44:45], s[44:45]
	s_or_b64 exec, exec, s[44:45]
	s_waitcnt lgkmcnt(5)
	v_mfma_f32_32x32x16_f16 v[42:57], v[78:81], v[22:25], v[42:57]
	ds_read_b128 v[38:41], v202 offset:15840
	ds_read_b128 v[22:25], v203 offset:15840
	s_mov_b64 s[44:45], s[40:41]
	ds_write_b128 v193, v[10:13] offset:16
	ds_write_b32 v193, v159 offset:548
	s_waitcnt lgkmcnt(8)
	v_mfma_f32_32x32x16_f16 v[42:57], v[58:61], v[18:21], v[42:57]
	s_and_saveexec_b64 s[46:47], s[8:9]
	s_andn2_b64 s[44:45], s[40:41], exec
	s_and_b64 s[48:49], s[10:11], exec
	s_or_b64 s[44:45], s[44:45], s[48:49]
	ds_write_b32 v193, v159 offset:536
	s_or_b64 exec, exec, s[46:47]
	s_and_saveexec_b64 s[46:47], s[44:45]
	ds_write_b32 v193, v159 offset:560
	s_or_b64 exec, exec, s[46:47]
	s_waitcnt lgkmcnt(5)
	v_mfma_f32_32x32x16_f16 v[42:57], v[70:73], v[26:29], v[42:57]
	s_waitcnt lgkmcnt(4)
	v_mfma_f32_32x32x16_f16 v[42:57], v[62:65], v[14:17], v[42:57]
	s_and_saveexec_b64 s[44:45], s[4:5]
	s_cbranch_execz .LBB6_83
	s_mov_b64 s[48:49], s[40:41]
	ds_write_b128 v200, v[6:9] offset:16
	ds_write_b32 v200, v160 offset:548
	s_and_saveexec_b64 s[46:47], s[8:9]
	s_andn2_b64 s[48:49], s[40:41], exec
	s_and_b64 s[50:51], s[10:11], exec
	s_or_b64 s[48:49], s[48:49], s[50:51]
	ds_write_b32 v200, v160 offset:536
	s_or_b64 exec, exec, s[46:47]
	s_and_b64 exec, exec, s[48:49]
	ds_write_b32 v200, v160 offset:560

.LBB6_88:
	s_or_b64 exec, exec, s[44:45]
	v_mov_b32_e32 v169, 0
	v_mov_b32_e32 v174, 0
	v_mov_b32_e32 v38, 0
	v_mov_b32_e32 v39, 0
	v_mov_b32_e32 v40, 0
	v_mov_b32_e32 v41, 0
	s_and_saveexec_b64 s[44:45], s[34:35]
	s_cbranch_execz .LBB6_90
	v_mov_b32_e32 v3, 0
	v_or_b32_e32 v2, 0x240, v166
	v_mov_b32_e32 v167, v3
	v_lshl_add_u64 v[4:5], v[2:3], 4, s[20:21]
	v_lshl_add_u64 v[2:3], v[166:167], 2, s[22:23]
	global_load_dwordx4 v[38:41], v[4:5], off
	global_load_dword v174, v[2:3], off offset:2304

.LBB6_96:
	s_or_b64 exec, exec, s[44:45]
	s_waitcnt lgkmcnt(0)
	s_barrier
	ds_read_b128 v[2:5], v195
	ds_read_b128 v[54:57], v196
	ds_read_b128 v[154:157], v195 offset:1056
	ds_read_b128 v[158:161], v195 offset:2112
	ds_read_b128 v[162:165], v196 offset:1056
	ds_read_b128 v[210:213], v196 offset:2112
	s_waitcnt lgkmcnt(5)
	v_mfma_f32_32x32x16_f16 v[2:17], v[150:153], v[2:5], 0
	s_waitcnt lgkmcnt(4)
	v_mfma_f32_32x32x16_f16 v[2:17], v[146:149], v[54:57], v[2:17]
	s_waitcnt lgkmcnt(3)
	v_mfma_f32_32x32x16_f16 v[2:17], v[142:145], v[154:157], v[2:17]
	ds_read_b128 v[54:57], v195 offset:3168
	ds_read_b128 v[154:157], v196 offset:3168
	s_waitcnt lgkmcnt(3)
	v_mfma_f32_32x32x16_f16 v[2:17], v[134:137], v[162:165], v[2:17]
	v_mfma_f32_32x32x16_f16 v[2:17], v[138:141], v[158:161], v[2:17]
	ds_read_b128 v[158:161], v195 offset:4224
	ds_read_b128 v[162:165], v196 offset:4224
	s_waitcnt lgkmcnt(4)
	v_mfma_f32_32x32x16_f16 v[2:17], v[130:133], v[210:213], v[2:17]
	s_waitcnt lgkmcnt(3)
	v_mfma_f32_32x32x16_f16 v[2:17], v[126:129], v[54:57], v[2:17]
	ds_read_b128 v[54:57], v195 offset:5280
	ds_read_b128 v[210:213], v196 offset:5280
	s_waitcnt lgkmcnt(4)
	v_mfma_f32_32x32x16_f16 v[2:17], v[118:121], v[154:157], v[2:17]
	s_waitcnt lgkmcnt(3)
	v_mfma_f32_32x32x16_f16 v[2:17], v[122:125], v[158:161], v[2:17]
	ds_read_b128 v[154:157], v195 offset:10560
	ds_read_b128 v[214:217], v196 offset:10560
	s_waitcnt lgkmcnt(4)
	v_mfma_f32_32x32x16_f16 v[2:17], v[110:113], v[162:165], v[2:17]
	s_waitcnt lgkmcnt(3)
	v_mfma_f32_32x32x16_f16 v[2:17], v[114:117], v[54:57], v[2:17]
	ds_read_b128 v[54:57], v195 offset:11616
	ds_read_b128 v[218:221], v196 offset:11616
	s_waitcnt lgkmcnt(4)
	v_mfma_f32_32x32x16_f16 v[2:17], v[102:105], v[210:213], v[2:17]
	s_waitcnt lgkmcnt(3)
	v_mfma_f32_32x32x16_f16 v[2:17], v[106:109], v[154:157], v[2:17]
	ds_read_b128 v[158:161], v195 offset:12672
	ds_read_b128 v[162:165], v196 offset:12672
	s_waitcnt lgkmcnt(4)
	v_mfma_f32_32x32x16_f16 v[2:17], v[98:101], v[214:217], v[2:17]
	s_waitcnt lgkmcnt(3)
	v_mfma_f32_32x32x16_f16 v[2:17], v[94:97], v[54:57], v[2:17]
	ds_read_b128 v[154:157], v195 offset:13728
	ds_read_b128 v[54:57], v196 offset:13728
	s_mov_b64 s[44:45], s[40:41]
	s_waitcnt vmcnt(1)
	ds_write_b128 v192, v[38:41] offset:63376
	s_waitcnt vmcnt(0)
	ds_write_b32 v192, v174 offset:63908
	s_waitcnt lgkmcnt(6)
	v_mfma_f32_32x32x16_f16 v[2:17], v[86:89], v[218:221], v[2:17]
	s_and_saveexec_b64 s[46:47], s[8:9]
	s_andn2_b64 s[44:45], s[40:41], exec
	s_and_b64 s[48:49], s[10:11], exec
	s_or_b64 s[44:45], s[44:45], s[48:49]
	ds_write_b32 v192, v174 offset:63896
	s_or_b64 exec, exec, s[46:47]
	s_and_saveexec_b64 s[46:47], s[44:45]
	ds_write_b32 v192, v174 offset:63920
	s_or_b64 exec, exec, s[46:47]
	s_waitcnt lgkmcnt(5)
	v_mfma_f32_32x32x16_f16 v[2:17], v[90:93], v[158:161], v[2:17]
	ds_read_b128 v[158:161], v195 offset:14784
	ds_read_b128 v[38:41], v196 offset:14784
	s_waitcnt lgkmcnt(6)
	v_mfma_f32_32x32x16_f16 v[2:17], v[82:85], v[162:165], v[2:17]
	s_and_saveexec_b64 s[44:45], s[14:15]
	s_xor_b64 s[44:45], exec, s[44:45]
	v_add_f32_e32 v35, 0, v35
	v_add_f32_e32 v34, 0, v34
	v_add_f32_e32 v34, v34, v50
	v_add_f32_e32 v35, v35, v51
	ds_write2st64_b32 v199, v34, v35 offset0:4 offset1:5
	s_andn2_saveexec_b64 s[44:45], s[44:45]
	s_or_b64 exec, exec, s[44:45]
	s_and_saveexec_b64 s[44:45], s[14:15]
	s_xor_b64 s[44:45], exec, s[44:45]
	v_add_f32_e32 v34, 0, v37
	v_add_f32_e32 v35, 0, v36
	v_add_f32_e32 v35, v35, v52
	v_add_f32_e32 v34, v34, v53
	ds_write2st64_b32 v199, v35, v34 offset0:6 offset1:7
	s_andn2_saveexec_b64 s[44:45], s[44:45]
	s_or_b64 exec, exec, s[44:45]
	s_waitcnt lgkmcnt(5)
	v_mfma_f32_32x32x16_f16 v[2:17], v[78:81], v[154:157], v[2:17]
	ds_read_b128 v[50:53], v195 offset:15840
	ds_read_b128 v[34:37], v196 offset:15840
	s_mov_b64 s[44:45], s[40:41]
	ds_write_b128 v193, v[26:29] offset:63376
	ds_write_b32 v193, v169 offset:63908
	s_waitcnt lgkmcnt(8)
	v_mfma_f32_32x32x16_f16 v[2:17], v[58:61], v[54:57], v[2:17]
	s_and_saveexec_b64 s[46:47], s[8:9]
	s_andn2_b64 s[44:45], s[40:41], exec
	s_and_b64 s[48:49], s[10:11], exec
	s_or_b64 s[44:45], s[44:45], s[48:49]
	ds_write_b32 v193, v169 offset:63896
	s_or_b64 exec, exec, s[46:47]
	s_and_saveexec_b64 s[46:47], s[44:45]
	ds_write_b32 v193, v169 offset:63920
	s_or_b64 exec, exec, s[46:47]
	s_waitcnt lgkmcnt(5)
	v_mfma_f32_32x32x16_f16 v[2:17], v[70:73], v[158:161], v[2:17]
	s_waitcnt lgkmcnt(4)
	v_mfma_f32_32x32x16_f16 v[2:17], v[62:65], v[38:41], v[2:17]
	s_and_saveexec_b64 s[44:45], s[4:5]
	s_cbranch_execz .LBB6_113
	s_mov_b64 s[48:49], s[40:41]
	ds_write_b128 v200, v[22:25] offset:63376
	ds_write_b32 v200, v171 offset:63908
	s_and_saveexec_b64 s[46:47], s[8:9]
	s_andn2_b64 s[48:49], s[40:41], exec
	s_and_b64 s[50:51], s[10:11], exec
	s_or_b64 s[48:49], s[48:49], s[50:51]
	ds_write_b32 v200, v171 offset:63896
	s_or_b64 exec, exec, s[46:47]
	s_and_b64 exec, exec, s[48:49]
	ds_write_b32 v200, v171 offset:63920

.LBB6_118:
	s_or_b64 exec, exec, s[44:45]
	v_mov_b32_e32 v174, 0
	v_mov_b32_e32 v176, 0
	v_mov_b32_e32 v54, 0
	v_mov_b32_e32 v55, 0
	v_mov_b32_e32 v56, 0
	v_mov_b32_e32 v57, 0
	s_and_saveexec_b64 s[44:45], s[34:35]
	s_cbranch_execz .LBB6_120
	v_mov_b32_e32 v15, 0
	v_or_b32_e32 v14, 0x260, v166
	v_mov_b32_e32 v167, v15
	v_lshl_add_u64 v[16:17], v[14:15], 4, s[20:21]
	v_lshl_add_u64 v[14:15], v[166:167], 2, s[22:23]
	global_load_dwordx4 v[54:57], v[16:17], off
	global_load_dword v176, v[14:15], off offset:2432

.LBB6_126:
	s_or_b64 exec, exec, s[16:17]
	s_waitcnt lgkmcnt(0)
	s_barrier
	ds_read_b128 v[14:17], v195 offset:63360
	ds_read_b128 v[154:157], v196 offset:63360
	ds_read_b128 v[158:161], v195 offset:64416
	ds_read_b128 v[162:165], v195 offset:65472
	ds_read_b128 v[166:169], v196 offset:64416
	ds_read_b128 v[210:213], v196 offset:65472
	s_waitcnt lgkmcnt(5)
	v_mfma_f32_32x32x16_f16 v[14:29], v[150:153], v[14:17], 0
	s_waitcnt lgkmcnt(4)
	v_mfma_f32_32x32x16_f16 v[14:29], v[146:149], v[154:157], v[14:29]
	s_waitcnt lgkmcnt(3)
	v_mfma_f32_32x32x16_f16 v[14:29], v[142:145], v[158:161], v[14:29]
	ds_read_b128 v[154:157], v202 offset:3168
	ds_read_b128 v[158:161], v203 offset:3168
	s_waitcnt lgkmcnt(3)
	v_mfma_f32_32x32x16_f16 v[14:29], v[134:137], v[166:169], v[14:29]
	v_mfma_f32_32x32x16_f16 v[14:29], v[138:141], v[162:165], v[14:29]
	ds_read_b128 v[162:165], v202 offset:4224
	ds_read_b128 v[166:169], v203 offset:4224
	s_waitcnt lgkmcnt(4)
	v_mfma_f32_32x32x16_f16 v[14:29], v[130:133], v[210:213], v[14:29]
	s_waitcnt lgkmcnt(3)
	v_mfma_f32_32x32x16_f16 v[14:29], v[126:129], v[154:157], v[14:29]
	ds_read_b128 v[154:157], v202 offset:5280
	ds_read_b128 v[210:213], v203 offset:5280
	s_waitcnt lgkmcnt(4)
	v_mfma_f32_32x32x16_f16 v[14:29], v[118:121], v[158:161], v[14:29]
	s_waitcnt lgkmcnt(3)
	v_mfma_f32_32x32x16_f16 v[14:29], v[122:125], v[162:165], v[14:29]
	ds_read_b128 v[158:161], v202 offset:10560
	ds_read_b128 v[214:217], v203 offset:10560
	s_waitcnt lgkmcnt(4)
	v_mfma_f32_32x32x16_f16 v[14:29], v[110:113], v[166:169], v[14:29]
	s_waitcnt lgkmcnt(3)
	v_mfma_f32_32x32x16_f16 v[14:29], v[114:117], v[154:157], v[14:29]
	ds_read_b128 v[154:157], v202 offset:11616
	ds_read_b128 v[218:221], v203 offset:11616
	s_waitcnt lgkmcnt(4)
	v_mfma_f32_32x32x16_f16 v[14:29], v[102:105], v[210:213], v[14:29]
	s_waitcnt lgkmcnt(3)
	v_mfma_f32_32x32x16_f16 v[14:29], v[106:109], v[158:161], v[14:29]
	ds_read_b128 v[162:165], v202 offset:12672
	ds_read_b128 v[166:169], v203 offset:12672
	s_waitcnt lgkmcnt(4)
	v_mfma_f32_32x32x16_f16 v[14:29], v[98:101], v[214:217], v[14:29]
	s_waitcnt lgkmcnt(3)
	v_mfma_f32_32x32x16_f16 v[14:29], v[94:97], v[154:157], v[14:29]
	ds_read_b128 v[158:161], v202 offset:13728
	ds_read_b128 v[154:157], v203 offset:13728
	s_mov_b64 s[16:17], s[40:41]
	s_waitcnt vmcnt(1)
	ds_write_b128 v192, v[54:57] offset:16
	s_waitcnt vmcnt(0)
	ds_write_b32 v192, v176 offset:548
	s_waitcnt lgkmcnt(6)
	v_mfma_f32_32x32x16_f16 v[14:29], v[86:89], v[218:221], v[14:29]
	s_and_saveexec_b64 s[42:43], s[8:9]
	s_andn2_b64 s[16:17], s[40:41], exec
	s_and_b64 s[44:45], s[10:11], exec
	s_or_b64 s[16:17], s[16:17], s[44:45]
	ds_write_b32 v192, v176 offset:536
	s_or_b64 exec, exec, s[42:43]
	s_and_saveexec_b64 s[42:43], s[16:17]
	ds_write_b32 v192, v176 offset:560
	s_or_b64 exec, exec, s[42:43]
	v_add_f32_e32 v31, v31, v47
	v_add_f32_e32 v46, v30, v46
	s_waitcnt lgkmcnt(5)
	v_mfma_f32_32x32x16_f16 v[14:29], v[90:93], v[162:165], v[14:29]
	ds_read_b128 v[162:165], v202 offset:14784
	ds_read_b128 v[54:57], v203 offset:14784
	v_mov_b32_e32 v170, v10
	v_mov_b32_e32 v171, v42
	v_mov_b32_e32 v47, v6
	v_pk_add_f32 v[170:171], v[170:171], v[46:47]
	v_add_f32_e32 v209, v31, v11
	s_waitcnt lgkmcnt(6)
	v_mfma_f32_32x32x16_f16 v[14:29], v[82:85], v[166:169], v[14:29]
	s_and_saveexec_b64 s[16:17], s[14:15]
	s_xor_b64 s[16:17], exec, s[16:17]
	v_add_f32_e32 v209, v31, v11
	ds_write2st64_b32 v199, v170, v209 offset1:1
	s_andn2_saveexec_b64 s[16:17], s[16:17]
	s_or_b64 exec, exec, s[16:17]
	v_add_f32_e32 v6, v33, v49
	v_add_f32_e32 v10, v32, v48
	v_add_f32_e32 v211, v10, v12
	v_add_f32_e32 v210, v6, v13
	s_and_saveexec_b64 s[16:17], s[14:15]
	s_xor_b64 s[16:17], exec, s[16:17]
	v_add_f32_e32 v210, v6, v13
	ds_write2st64_b32 v199, v211, v210 offset0:2 offset1:3
	s_andn2_saveexec_b64 s[16:17], s[16:17]
	s_or_b64 exec, exec, s[16:17]
	s_waitcnt lgkmcnt(5)
	v_mfma_f32_32x32x16_f16 v[14:29], v[78:81], v[158:161], v[14:29]
	ds_read_b128 v[30:33], v202 offset:15840
	ds_read_b128 v[10:13], v203 offset:15840
	s_mov_b64 s[16:17], s[40:41]
	ds_write_b128 v193, v[50:53] offset:16
	ds_write_b32 v193, v174 offset:548
	s_waitcnt lgkmcnt(8)
	v_mfma_f32_32x32x16_f16 v[14:29], v[58:61], v[154:157], v[14:29]
	s_and_saveexec_b64 s[42:43], s[8:9]
	s_andn2_b64 s[16:17], s[40:41], exec
	s_and_b64 s[44:45], s[10:11], exec
	s_or_b64 s[16:17], s[16:17], s[44:45]
	ds_write_b32 v193, v174 offset:536
	s_or_b64 exec, exec, s[42:43]
	s_and_saveexec_b64 s[42:43], s[16:17]
	ds_write_b32 v193, v174 offset:560
	s_or_b64 exec, exec, s[42:43]
	s_waitcnt lgkmcnt(5)
	v_mfma_f32_32x32x16_f16 v[14:29], v[70:73], v[162:165], v[14:29]
	s_waitcnt lgkmcnt(4)
	v_mfma_f32_32x32x16_f16 v[14:29], v[62:65], v[54:57], v[14:29]
	s_and_saveexec_b64 s[16:17], s[4:5]
	s_cbranch_execz .LBB6_143
	s_mov_b64 s[44:45], s[40:41]
	ds_write_b128 v200, v[38:41] offset:16
	ds_write_b32 v200, v175 offset:548
	s_and_saveexec_b64 s[42:43], s[8:9]
	s_andn2_b64 s[44:45], s[40:41], exec
	s_and_b64 s[46:47], s[10:11], exec
	s_or_b64 s[44:45], s[44:45], s[46:47]
	ds_write_b32 v200, v175 offset:536
	s_or_b64 exec, exec, s[42:43]
	s_and_b64 exec, exec, s[44:45]
	ds_write_b32 v200, v175 offset:560

.LBB6_266:
	s_or_b64 exec, exec, s[12:13]
	v_mov_b32_e32 v154, 0
	v_mov_b32_e32 v46, 0
	v_mov_b32_e32 v14, 0
	v_mov_b32_e32 v15, 0
	v_mov_b32_e32 v16, 0
	v_mov_b32_e32 v17, 0
	s_and_saveexec_b64 s[12:13], s[34:35]
	s_cbranch_execz .LBB6_268
	s_lshl_b32 s14, s59, 10
	v_or3_b32 v2, v22, s14, v1
	v_lshl_or_b32 v2, v2, 10, v206
	v_mov_b32_e32 v3, 0
	v_lshl_add_u64 v[4:5], v[2:3], 4, s[20:21]
	v_lshl_add_u64 v[2:3], v[2:3], 2, s[22:23]
	global_load_dwordx4 v[14:17], v[4:5], off offset:512
	global_load_dword v46, v[2:3], off offset:128

.LBB6_274:
	s_or_b64 exec, exec, s[12:13]
	v_and_b32_e32 v192, 2, v194
	v_lshlrev_b32_e32 v19, 2, v194
	v_lshl_add_u32 v18, v186, 1, v192
	v_and_b32_e32 v193, 4, v19
	v_mad_u32_u24 v18, v18, 10, v193
	v_mul_u32_u24_e32 v26, 0x420, v18
	v_add_lshl_u32 v18, v190, v206, 4
	v_add3_u32 v195, v26, v18, 0
	s_waitcnt lgkmcnt(0)
	s_barrier
	ds_read_b128 v[18:21], v195 offset:63360
	v_mov_b32_e32 v22, 0x220
	v_cmp_gt_u32_e64 s[12:13], 32, v182
	v_add_u32_e32 v196, 0xf780, v195
	s_nop 0
	v_cndmask_b32_e64 v22, v22, 32, s[12:13]
	v_add_u32_e32 v27, v22, v167
	ds_read_b128 v[22:25], v195 offset:64416
	s_waitcnt vmcnt(23) lgkmcnt(1)
	v_mfma_f32_32x32x16_f16 v[30:45], v[54:57], v[18:21], 0
	v_add3_u32 v197, v27, v26, 0
	ds_read_b128 v[18:21], v197 offset:63360
	ds_read_b128 v[26:29], v195 offset:65472
	ds_read_b128 v[48:51], v197 offset:64416
	ds_read_b128 v[156:159], v197 offset:65472
	v_add_u32_e32 v198, 0xf780, v197
	s_waitcnt vmcnt(22) lgkmcnt(3)
	v_mfma_f32_32x32x16_f16 v[30:45], v[58:61], v[18:21], v[30:45]
	s_waitcnt vmcnt(21)
	v_mfma_f32_32x32x16_f16 v[30:45], v[62:65], v[22:25], v[30:45]
	ds_read_b128 v[18:21], v196 offset:3168
	ds_read_b128 v[22:25], v198 offset:3168
	s_waitcnt vmcnt(20) lgkmcnt(3)
	v_mfma_f32_32x32x16_f16 v[30:45], v[66:69], v[48:51], v[30:45]
	s_waitcnt vmcnt(19)
	v_mfma_f32_32x32x16_f16 v[30:45], v[70:73], v[26:29], v[30:45]
	ds_read_b128 v[26:29], v196 offset:4224
	ds_read_b128 v[48:51], v198 offset:4224
	s_waitcnt vmcnt(18) lgkmcnt(4)
	v_mfma_f32_32x32x16_f16 v[30:45], v[74:77], v[156:159], v[30:45]
	s_waitcnt vmcnt(17) lgkmcnt(3)
	v_mfma_f32_32x32x16_f16 v[30:45], v[78:81], v[18:21], v[30:45]
	ds_read_b128 v[18:21], v196 offset:5280
	ds_read_b128 v[156:159], v198 offset:5280
	s_waitcnt vmcnt(16) lgkmcnt(4)
	v_mfma_f32_32x32x16_f16 v[30:45], v[82:85], v[22:25], v[30:45]
	s_waitcnt vmcnt(15) lgkmcnt(3)
	v_mfma_f32_32x32x16_f16 v[30:45], v[86:89], v[26:29], v[30:45]
	ds_read_b128 v[22:25], v196 offset:10560
	ds_read_b128 v[160:163], v198 offset:10560
	s_waitcnt vmcnt(14) lgkmcnt(4)
	v_mfma_f32_32x32x16_f16 v[30:45], v[90:93], v[48:51], v[30:45]
	s_waitcnt vmcnt(13) lgkmcnt(3)
	v_mfma_f32_32x32x16_f16 v[30:45], v[94:97], v[18:21], v[30:45]
	ds_read_b128 v[18:21], v196 offset:11616
	ds_read_b128 v[174:177], v198 offset:11616
	s_waitcnt vmcnt(12) lgkmcnt(4)
	v_mfma_f32_32x32x16_f16 v[30:45], v[98:101], v[156:159], v[30:45]
	s_waitcnt vmcnt(11) lgkmcnt(3)
	v_mfma_f32_32x32x16_f16 v[30:45], v[102:105], v[22:25], v[30:45]
	ds_read_b128 v[26:29], v196 offset:12672
	ds_read_b128 v[50:53], v198 offset:12672
	s_waitcnt vmcnt(10) lgkmcnt(4)
	v_mfma_f32_32x32x16_f16 v[30:45], v[106:109], v[160:163], v[30:45]
	s_waitcnt vmcnt(9) lgkmcnt(3)
	v_mfma_f32_32x32x16_f16 v[30:45], v[110:113], v[18:21], v[30:45]
	ds_read_b128 v[18:21], v196 offset:13728
	ds_read_b128 v[22:25], v198 offset:13728
	s_mov_b64 s[12:13], s[24:25]
	s_waitcnt vmcnt(1)
	ds_write_b128 v188, v[14:17] offset:16
	s_waitcnt vmcnt(0)
	ds_write_b32 v188, v46 offset:548
	s_waitcnt lgkmcnt(6)
	v_mfma_f32_32x32x16_f16 v[30:45], v[114:117], v[174:177], v[30:45]
	s_and_saveexec_b64 s[14:15], s[8:9]
	s_andn2_b64 s[12:13], s[24:25], exec
	s_and_b64 s[26:27], s[10:11], exec
	s_or_b64 s[12:13], s[12:13], s[26:27]
	ds_write_b32 v188, v46 offset:536
	s_or_b64 exec, exec, s[14:15]
	s_and_saveexec_b64 s[14:15], s[12:13]
	ds_write_b32 v188, v46 offset:560
	s_or_b64 exec, exec, s[14:15]
	s_waitcnt lgkmcnt(5)
	v_mfma_f32_32x32x16_f16 v[30:45], v[118:121], v[26:29], v[30:45]
	ds_read_b128 v[46:49], v196 offset:14784
	ds_read_b128 v[26:29], v198 offset:14784
	v_cmp_eq_u32_e64 s[12:13], 0, v186
	v_cmp_ne_u32_e64 s[14:15], 0, v186
	v_lshlrev_b32_e32 v171, 11, v194
	v_lshlrev_b32_e32 v174, 2, v182
	s_waitcnt lgkmcnt(6)
	v_mfma_f32_32x32x16_f16 v[30:45], v[122:125], v[50:53], v[30:45]
	s_and_saveexec_b64 s[26:27], s[14:15]
	s_cbranch_execz .LBB6_280
	s_add_i32 s42, 0, 0x1ef00
	v_add3_u32 v14, s42, v171, v174
	v_mov_b32_e32 v15, 0
	ds_write2st64_b32 v14, v15, v15 offset1:1
	ds_write2st64_b32 v14, v15, v15 offset0:2 offset1:3

.LBB6_294:
	s_or_b64 exec, exec, s[26:27]
	s_lshl_b32 s53, s59, 10
	v_add_lshl_u32 v2, v1, s53, 10
	v_lshl_add_u32 v2, v185, 15, v2
	v_or_b32_e32 v158, v2, v206
	v_mov_b32_e32 v161, 0
	v_mov_b32_e32 v175, 0
	s_nop 2
	v_mov_b32_e32 v42, 0
	v_mov_b32_e32 v43, 0
	v_mov_b32_e32 v44, 0
	v_mov_b32_e32 v45, 0
	s_and_saveexec_b64 s[26:27], s[34:35]
	s_cbranch_execz .LBB6_296
	v_mov_b32_e32 v159, 0
	v_lshl_add_u64 v[2:3], v[158:159], 4, s[20:21]
	global_load_dwordx4 v[42:45], v[2:3], off offset:1024
	v_lshl_add_u64 v[2:3], v[158:159], 2, s[22:23]
	global_load_dword v175, v[2:3], off offset:256

.LBB6_302:
	s_or_b64 exec, exec, s[26:27]
	s_waitcnt lgkmcnt(0)
	s_barrier
	ds_read_b128 v[2:5], v195
	ds_read_b128 v[46:49], v197
	ds_read_b128 v[50:53], v195 offset:1056
	ds_read_b128 v[150:153], v195 offset:2112
	ds_read_b128 v[154:157], v197 offset:1056
	ds_read_b128 v[202:205], v197 offset:2112
	s_waitcnt lgkmcnt(5)
	v_mfma_f32_32x32x16_f16 v[2:17], v[54:57], v[2:5], 0
	s_waitcnt lgkmcnt(4)
	v_mfma_f32_32x32x16_f16 v[2:17], v[58:61], v[46:49], v[2:17]
	s_waitcnt lgkmcnt(3)
	v_mfma_f32_32x32x16_f16 v[2:17], v[62:65], v[50:53], v[2:17]
	ds_read_b128 v[46:49], v195 offset:3168
	ds_read_b128 v[50:53], v197 offset:3168
	s_waitcnt lgkmcnt(3)
	v_mfma_f32_32x32x16_f16 v[2:17], v[66:69], v[154:157], v[2:17]
	v_mfma_f32_32x32x16_f16 v[2:17], v[70:73], v[150:153], v[2:17]
	ds_read_b128 v[150:153], v195 offset:4224
	ds_read_b128 v[154:157], v197 offset:4224
	s_waitcnt lgkmcnt(4)
	v_mfma_f32_32x32x16_f16 v[2:17], v[74:77], v[202:205], v[2:17]
	s_waitcnt lgkmcnt(3)
	v_mfma_f32_32x32x16_f16 v[2:17], v[78:81], v[46:49], v[2:17]
	ds_read_b128 v[46:49], v195 offset:5280
	ds_read_b128 v[202:205], v197 offset:5280
	s_waitcnt lgkmcnt(4)
	v_mfma_f32_32x32x16_f16 v[2:17], v[82:85], v[50:53], v[2:17]
	s_waitcnt lgkmcnt(3)
	v_mfma_f32_32x32x16_f16 v[2:17], v[86:89], v[150:153], v[2:17]
	ds_read_b128 v[50:53], v195 offset:10560
	ds_read_b128 v[208:211], v197 offset:10560
	s_waitcnt lgkmcnt(4)
	v_mfma_f32_32x32x16_f16 v[2:17], v[90:93], v[154:157], v[2:17]
	s_waitcnt lgkmcnt(3)
	v_mfma_f32_32x32x16_f16 v[2:17], v[94:97], v[46:49], v[2:17]
	ds_read_b128 v[46:49], v195 offset:11616
	ds_read_b128 v[212:215], v197 offset:11616
	s_waitcnt lgkmcnt(4)
	v_mfma_f32_32x32x16_f16 v[2:17], v[98:101], v[202:205], v[2:17]
	s_waitcnt lgkmcnt(3)
	v_mfma_f32_32x32x16_f16 v[2:17], v[102:105], v[50:53], v[2:17]
	ds_read_b128 v[150:153], v195 offset:12672
	ds_read_b128 v[154:157], v197 offset:12672
	s_waitcnt lgkmcnt(4)
	v_mfma_f32_32x32x16_f16 v[2:17], v[106:109], v[208:211], v[2:17]
	s_waitcnt lgkmcnt(3)
	v_mfma_f32_32x32x16_f16 v[2:17], v[110:113], v[46:49], v[2:17]
	ds_read_b128 v[50:53], v195 offset:13728
	ds_read_b128 v[46:49], v197 offset:13728
	s_mov_b64 s[26:27], s[24:25]
	s_waitcnt vmcnt(1)
	ds_write_b128 v188, v[42:45] offset:63376
	s_waitcnt vmcnt(0)
	ds_write_b32 v188, v175 offset:63908
	s_waitcnt lgkmcnt(6)
	v_mfma_f32_32x32x16_f16 v[2:17], v[114:117], v[212:215], v[2:17]
	s_and_saveexec_b64 s[42:43], s[8:9]
	s_andn2_b64 s[26:27], s[24:25], exec
	s_and_b64 s[44:45], s[10:11], exec
	s_or_b64 s[26:27], s[26:27], s[44:45]
	ds_write_b32 v188, v175 offset:63896
	s_or_b64 exec, exec, s[42:43]
	s_and_saveexec_b64 s[42:43], s[26:27]
	ds_write_b32 v188, v175 offset:63920
	s_or_b64 exec, exec, s[42:43]
	s_add_i32 s26, 0, 0x1ef00
	v_add3_u32 v185, s26, v171, v174
	s_waitcnt lgkmcnt(5)
	v_mfma_f32_32x32x16_f16 v[2:17], v[118:121], v[150:153], v[2:17]
	ds_read_b128 v[150:153], v195 offset:14784
	ds_read_b128 v[42:45], v197 offset:14784
	s_waitcnt lgkmcnt(6)
	v_mfma_f32_32x32x16_f16 v[2:17], v[122:125], v[154:157], v[2:17]
	s_and_saveexec_b64 s[26:27], s[14:15]
	s_xor_b64 s[26:27], exec, s[26:27]
	v_add_f32_e32 v38, 0, v38
	v_add_f32_e32 v39, 0, v39
	ds_write2st64_b32 v185, v38, v39 offset0:4 offset1:5
	s_andn2_saveexec_b64 s[26:27], s[26:27]
	s_or_b64 exec, exec, s[26:27]
	s_and_saveexec_b64 s[26:27], s[14:15]
	s_xor_b64 s[26:27], exec, s[26:27]
	v_add_f32_e32 v38, 0, v40
	v_add_f32_e32 v39, 0, v41
	ds_write2st64_b32 v185, v38, v39 offset0:6 offset1:7
	s_andn2_saveexec_b64 s[26:27], s[26:27]
	s_or_b64 exec, exec, s[26:27]
	s_waitcnt lgkmcnt(5)
	v_mfma_f32_32x32x16_f16 v[2:17], v[126:129], v[50:53], v[2:17]
	ds_read_b128 v[50:53], v195 offset:15840
	ds_read_b128 v[38:41], v197 offset:15840
	s_mov_b64 s[26:27], s[24:25]
	ds_write_b128 v189, v[26:29] offset:63376
	ds_write_b32 v189, v161 offset:63908
	s_waitcnt lgkmcnt(8)
	v_mfma_f32_32x32x16_f16 v[2:17], v[130:133], v[46:49], v[2:17]
	s_and_saveexec_b64 s[42:43], s[8:9]
	s_andn2_b64 s[26:27], s[24:25], exec
	s_and_b64 s[44:45], s[10:11], exec
	s_or_b64 s[26:27], s[26:27], s[44:45]
	ds_write_b32 v189, v161 offset:63896
	s_or_b64 exec, exec, s[42:43]
	s_and_saveexec_b64 s[42:43], s[26:27]
	ds_write_b32 v189, v161 offset:63920
	s_or_b64 exec, exec, s[42:43]
	s_movk_i32 s26, 0x420
	v_mad_u32_u24 v26, v166, s26, 0
	s_waitcnt lgkmcnt(5)
	v_mfma_f32_32x32x16_f16 v[2:17], v[134:137], v[150:153], v[2:17]
	v_add_u32_e32 v186, v26, v167
	s_waitcnt lgkmcnt(4)
	v_mfma_f32_32x32x16_f16 v[2:17], v[138:141], v[42:45], v[2:17]
	s_and_saveexec_b64 s[26:27], s[4:5]
	s_cbranch_execz .LBB6_319
	s_mov_b64 s[44:45], s[24:25]
	ds_write_b128 v186, v[22:25] offset:63376
	ds_write_b32 v186, v163 offset:63908
	s_and_saveexec_b64 s[42:43], s[8:9]
	s_andn2_b64 s[44:45], s[24:25], exec
	s_and_b64 s[46:47], s[10:11], exec
	s_or_b64 s[44:45], s[44:45], s[46:47]
	ds_write_b32 v186, v163 offset:63896
	s_or_b64 exec, exec, s[42:43]
	s_and_b64 exec, exec, s[44:45]
	ds_write_b32 v186, v163 offset:63920

.LBB6_324:
	s_or_b64 exec, exec, s[26:27]
	v_mov_b32_e32 v167, 0
	v_mov_b32_e32 v170, 0
	v_mov_b32_e32 v50, 0
	v_mov_b32_e32 v51, 0
	v_mov_b32_e32 v52, 0
	v_mov_b32_e32 v53, 0
	s_and_saveexec_b64 s[26:27], s[34:35]
	s_cbranch_execz .LBB6_326
	v_mov_b32_e32 v159, 0
	v_lshl_add_u64 v[14:15], v[158:159], 4, s[20:21]
	global_load_dwordx4 v[50:53], v[14:15], off offset:1536
	v_lshl_add_u64 v[14:15], v[158:159], 2, s[22:23]
	global_load_dword v170, v[14:15], off offset:384

.LBB6_332:
	s_or_b64 exec, exec, s[16:17]
	s_waitcnt lgkmcnt(0)
	s_barrier
	ds_read_b128 v[14:17], v195 offset:63360
	ds_read_b128 v[150:153], v197 offset:63360
	ds_read_b128 v[154:157], v195 offset:64416
	ds_read_b128 v[158:161], v195 offset:65472
	ds_read_b128 v[162:165], v197 offset:64416
	ds_read_b128 v[202:205], v197 offset:65472
	s_waitcnt lgkmcnt(5)
	v_mfma_f32_32x32x16_f16 v[14:29], v[54:57], v[14:17], 0
	s_waitcnt lgkmcnt(4)
	v_mfma_f32_32x32x16_f16 v[14:29], v[58:61], v[150:153], v[14:29]
	s_waitcnt lgkmcnt(3)
	v_mfma_f32_32x32x16_f16 v[14:29], v[62:65], v[154:157], v[14:29]
	ds_read_b128 v[150:153], v196 offset:3168
	ds_read_b128 v[154:157], v198 offset:3168
	s_waitcnt lgkmcnt(3)
	v_mfma_f32_32x32x16_f16 v[14:29], v[66:69], v[162:165], v[14:29]
	v_mfma_f32_32x32x16_f16 v[14:29], v[70:73], v[158:161], v[14:29]
	ds_read_b128 v[158:161], v196 offset:4224
	ds_read_b128 v[162:165], v198 offset:4224
	s_waitcnt lgkmcnt(4)
	v_mfma_f32_32x32x16_f16 v[14:29], v[74:77], v[202:205], v[14:29]
	s_waitcnt lgkmcnt(3)
	v_mfma_f32_32x32x16_f16 v[14:29], v[78:81], v[150:153], v[14:29]
	ds_read_b128 v[150:153], v196 offset:5280
	ds_read_b128 v[202:205], v198 offset:5280
	s_waitcnt lgkmcnt(4)
	v_mfma_f32_32x32x16_f16 v[14:29], v[82:85], v[154:157], v[14:29]
	s_waitcnt lgkmcnt(3)
	v_mfma_f32_32x32x16_f16 v[14:29], v[86:89], v[158:161], v[14:29]
	ds_read_b128 v[154:157], v196 offset:10560
	ds_read_b128 v[208:211], v198 offset:10560
	s_waitcnt lgkmcnt(4)
	v_mfma_f32_32x32x16_f16 v[14:29], v[90:93], v[162:165], v[14:29]
	s_waitcnt lgkmcnt(3)
	v_mfma_f32_32x32x16_f16 v[14:29], v[94:97], v[150:153], v[14:29]
	ds_read_b128 v[150:153], v196 offset:11616
	ds_read_b128 v[212:215], v198 offset:11616
	s_waitcnt lgkmcnt(4)
	v_mfma_f32_32x32x16_f16 v[14:29], v[98:101], v[202:205], v[14:29]
	s_waitcnt lgkmcnt(3)
	v_mfma_f32_32x32x16_f16 v[14:29], v[102:105], v[154:157], v[14:29]
	ds_read_b128 v[158:161], v196 offset:12672
	ds_read_b128 v[162:165], v198 offset:12672
	s_waitcnt lgkmcnt(4)
	v_mfma_f32_32x32x16_f16 v[14:29], v[106:109], v[208:211], v[14:29]
	s_waitcnt lgkmcnt(3)
	v_mfma_f32_32x32x16_f16 v[14:29], v[110:113], v[150:153], v[14:29]
	ds_read_b128 v[154:157], v196 offset:13728
	ds_read_b128 v[150:153], v198 offset:13728
	s_mov_b64 s[16:17], s[24:25]
	s_waitcnt vmcnt(1)
	ds_write_b128 v188, v[50:53] offset:16
	s_waitcnt vmcnt(0)
	ds_write_b32 v188, v170 offset:548
	s_waitcnt lgkmcnt(6)
	v_mfma_f32_32x32x16_f16 v[14:29], v[114:117], v[212:215], v[14:29]
	s_and_saveexec_b64 s[26:27], s[8:9]
	s_andn2_b64 s[16:17], s[24:25], exec
	s_and_b64 s[34:35], s[10:11], exec
	s_or_b64 s[16:17], s[16:17], s[34:35]
	ds_write_b32 v188, v170 offset:536
	s_or_b64 exec, exec, s[26:27]
	s_and_saveexec_b64 s[26:27], s[16:17]
	ds_write_b32 v188, v170 offset:560
	s_or_b64 exec, exec, s[26:27]
	v_add_f32_e32 v35, 0, v35
	v_add_f32_e32 v170, 0, v34
	s_waitcnt lgkmcnt(5)
	v_mfma_f32_32x32x16_f16 v[14:29], v[118:121], v[158:161], v[14:29]
	ds_read_b128 v[158:161], v196 offset:14784
	ds_read_b128 v[50:53], v198 offset:14784
	v_mov_b32_e32 v176, v10
	v_mov_b32_e32 v177, v30
	v_mov_b32_e32 v171, v6
	v_pk_add_f32 v[170:171], v[176:177], v[170:171]
	v_add_f32_e32 v205, v35, v11
	s_waitcnt lgkmcnt(6)
	v_mfma_f32_32x32x16_f16 v[14:29], v[122:125], v[162:165], v[14:29]
	s_and_saveexec_b64 s[16:17], s[14:15]
	s_xor_b64 s[16:17], exec, s[16:17]
	v_add_f32_e32 v205, v35, v11
	ds_write2st64_b32 v185, v170, v205 offset1:1
	s_andn2_saveexec_b64 s[16:17], s[16:17]
	s_or_b64 exec, exec, s[16:17]
	v_add_f32_e32 v6, 0, v37
	v_add_f32_e32 v10, 0, v36
	v_add_f32_e32 v208, v10, v12
	v_add_f32_e32 v207, v6, v13
	s_and_saveexec_b64 s[16:17], s[14:15]
	s_xor_b64 s[16:17], exec, s[16:17]
	v_add_f32_e32 v207, v6, v13
	ds_write2st64_b32 v185, v208, v207 offset0:2 offset1:3
	s_andn2_saveexec_b64 s[16:17], s[16:17]
	s_or_b64 exec, exec, s[16:17]
	s_waitcnt lgkmcnt(5)
	v_mfma_f32_32x32x16_f16 v[14:29], v[126:129], v[154:157], v[14:29]
	ds_read_b128 v[34:37], v196 offset:15840
	ds_read_b128 v[10:13], v198 offset:15840
	s_mov_b64 s[16:17], s[24:25]
	ds_write_b128 v189, v[46:49] offset:16
	ds_write_b32 v189, v167 offset:548
	s_waitcnt lgkmcnt(8)
	v_mfma_f32_32x32x16_f16 v[14:29], v[130:133], v[150:153], v[14:29]
	s_and_saveexec_b64 s[26:27], s[8:9]
	s_andn2_b64 s[16:17], s[24:25], exec
	s_and_b64 s[34:35], s[10:11], exec
	s_or_b64 s[16:17], s[16:17], s[34:35]
	ds_write_b32 v189, v167 offset:536
	s_or_b64 exec, exec, s[26:27]
	s_and_saveexec_b64 s[26:27], s[16:17]
	ds_write_b32 v189, v167 offset:560
	s_or_b64 exec, exec, s[26:27]
	s_waitcnt lgkmcnt(5)
	v_mfma_f32_32x32x16_f16 v[14:29], v[134:137], v[158:161], v[14:29]
	s_waitcnt lgkmcnt(4)
	v_mfma_f32_32x32x16_f16 v[14:29], v[138:141], v[50:53], v[14:29]
	s_and_saveexec_b64 s[16:17], s[4:5]
	s_cbranch_execz .LBB6_349
	s_mov_b64 s[34:35], s[24:25]
	ds_write_b128 v186, v[42:45] offset:16
	ds_write_b32 v186, v174 offset:548
	s_and_saveexec_b64 s[26:27], s[8:9]
	s_andn2_b64 s[34:35], s[24:25], exec
	s_and_b64 s[40:41], s[10:11], exec
	s_or_b64 s[34:35], s[34:35], s[40:41]
	ds_write_b32 v186, v174 offset:536
	s_or_b64 exec, exec, s[26:27]
	s_and_b64 exec, exec, s[34:35]
	ds_write_b32 v186, v174 offset:560

.LBB8_29:
	s_or_b64 exec, exec, s[10:11]
	s_lshl_b32 s56, s53, 10
	v_add_lshl_u32 v2, s56, v192, 10
	v_lshl_add_u32 v2, v196, 15, v2
	v_or_b32_e32 v166, v2, v190
	v_mov_b32_e32 v154, 0
	v_ashrrev_i32_e32 v167, 31, v166
	v_mov_b32_e32 v50, 0
	v_mov_b32_e32 v14, 0
	v_mov_b32_e32 v15, 0
	v_mov_b32_e32 v16, 0
	v_mov_b32_e32 v17, 0
	s_and_saveexec_b64 s[10:11], s[26:27]
	s_cbranch_execz .LBB8_31
	v_or_b32_e32 v2, 0x200, v166
	v_ashrrev_i32_e32 v3, 31, v2
	v_lshl_add_u64 v[2:3], v[2:3], 4, s[16:17]
	global_load_dwordx4 v[14:17], v[2:3], off
	v_lshl_add_u64 v[2:3], v[166:167], 2, s[18:19]
	global_load_dword v50, v[2:3], off offset:2048

.LBB8_37:
	s_or_b64 exec, exec, s[10:11]
	v_and_b32_e32 v208, 2, v198
	v_lshlrev_b32_e32 v19, 2, v198
	v_lshl_add_u32 v18, v199, 1, v208
	v_and_b32_e32 v207, 4, v19
	v_mad_u32_u24 v18, v18, 10, v207
	v_mul_u32_u24_e32 v22, 0x420, v18
	v_add_lshl_u32 v18, v191, v190, 4
	v_add3_u32 v204, v22, v18, 0
	s_waitcnt lgkmcnt(0)
	s_barrier
	ds_read_b128 v[18:21], v204
	v_mov_b32_e32 v23, 0x220
	s_waitcnt vmcnt(23) lgkmcnt(0)
	v_mfma_f32_32x32x16_f16 v[30:45], v[150:153], v[18:21], 0
	v_cmp_gt_u32_e64 s[10:11], 32, v197
	s_nop 1
	v_cndmask_b32_e64 v23, v23, 32, s[10:11]
	v_add_u32_e32 v18, v23, v55
	v_add3_u32 v205, v18, v22, 0
	ds_read_b128 v[18:21], v205
	ds_read_b128 v[22:25], v204 offset:1056
	ds_read_b128 v[26:29], v204 offset:2112
	ds_read_b128 v[46:49], v205 offset:1056
	ds_read_b128 v[156:159], v205 offset:2112
	s_waitcnt vmcnt(22) lgkmcnt(4)
	v_mfma_f32_32x32x16_f16 v[30:45], v[146:149], v[18:21], v[30:45]
	s_waitcnt vmcnt(21) lgkmcnt(3)
	v_mfma_f32_32x32x16_f16 v[30:45], v[142:145], v[22:25], v[30:45]
	ds_read_b128 v[18:21], v204 offset:3168
	ds_read_b128 v[22:25], v205 offset:3168
	s_waitcnt vmcnt(20) lgkmcnt(3)
	v_mfma_f32_32x32x16_f16 v[30:45], v[134:137], v[46:49], v[30:45]
	s_waitcnt vmcnt(19)
	v_mfma_f32_32x32x16_f16 v[30:45], v[138:141], v[26:29], v[30:45]
	ds_read_b128 v[26:29], v204 offset:4224
	ds_read_b128 v[46:49], v205 offset:4224
	s_waitcnt vmcnt(18) lgkmcnt(4)
	v_mfma_f32_32x32x16_f16 v[30:45], v[130:133], v[156:159], v[30:45]
	s_waitcnt vmcnt(17) lgkmcnt(3)
	v_mfma_f32_32x32x16_f16 v[30:45], v[126:129], v[18:21], v[30:45]
	ds_read_b128 v[18:21], v204 offset:5280
	ds_read_b128 v[156:159], v205 offset:5280
	s_waitcnt vmcnt(16) lgkmcnt(4)
	v_mfma_f32_32x32x16_f16 v[30:45], v[118:121], v[22:25], v[30:45]
	s_waitcnt vmcnt(15) lgkmcnt(3)
	v_mfma_f32_32x32x16_f16 v[30:45], v[122:125], v[26:29], v[30:45]
	ds_read_b128 v[22:25], v204 offset:10560
	ds_read_b128 v[160:163], v205 offset:10560
	s_waitcnt vmcnt(14) lgkmcnt(4)
	v_mfma_f32_32x32x16_f16 v[30:45], v[110:113], v[46:49], v[30:45]
	s_waitcnt vmcnt(13) lgkmcnt(3)
	v_mfma_f32_32x32x16_f16 v[30:45], v[114:117], v[18:21], v[30:45]
	ds_read_b128 v[46:49], v204 offset:11616
	ds_read_b128 v[184:187], v205 offset:11616
	s_waitcnt vmcnt(12) lgkmcnt(4)
	v_mfma_f32_32x32x16_f16 v[30:45], v[102:105], v[156:159], v[30:45]
	s_waitcnt vmcnt(11) lgkmcnt(3)
	v_mfma_f32_32x32x16_f16 v[30:45], v[106:109], v[22:25], v[30:45]
	ds_read_b128 v[26:29], v204 offset:12672
	ds_read_b128 v[18:21], v205 offset:12672
	s_waitcnt vmcnt(10) lgkmcnt(4)
	v_mfma_f32_32x32x16_f16 v[30:45], v[98:101], v[160:163], v[30:45]
	s_waitcnt vmcnt(9) lgkmcnt(3)
	v_mfma_f32_32x32x16_f16 v[30:45], v[94:97], v[46:49], v[30:45]
	ds_read_b128 v[46:49], v204 offset:13728
	ds_read_b128 v[22:25], v205 offset:13728
	s_mov_b64 s[10:11], s[34:35]
	s_waitcnt vmcnt(1)
	ds_write_b128 v202, v[14:17] offset:63376
	s_waitcnt vmcnt(0)
	ds_write_b32 v202, v50 offset:63908
	s_waitcnt lgkmcnt(6)
	v_mfma_f32_32x32x16_f16 v[30:45], v[86:89], v[184:187], v[30:45]
	s_and_saveexec_b64 s[12:13], s[6:7]
	s_andn2_b64 s[10:11], s[34:35], exec
	s_and_b64 s[38:39], s[8:9], exec
	s_or_b64 s[10:11], s[10:11], s[38:39]
	ds_write_b32 v202, v50 offset:63896
	s_or_b64 exec, exec, s[12:13]
	s_and_saveexec_b64 s[12:13], s[10:11]
	ds_write_b32 v202, v50 offset:63920
	s_or_b64 exec, exec, s[12:13]
	s_waitcnt lgkmcnt(5)
	v_mfma_f32_32x32x16_f16 v[30:45], v[90:93], v[26:29], v[30:45]
	ds_read_b128 v[50:53], v204 offset:14784
	ds_read_b128 v[26:29], v205 offset:14784
	s_waitcnt lgkmcnt(6)
	v_mfma_f32_32x32x16_f16 v[30:45], v[82:85], v[18:21], v[30:45]
	s_waitcnt lgkmcnt(5)
	v_mfma_f32_32x32x16_f16 v[30:45], v[78:81], v[46:49], v[30:45]
	ds_read_b128 v[18:21], v204 offset:15840
	ds_read_b128 v[14:17], v205 offset:15840
	s_mov_b64 s[10:11], s[34:35]
	ds_write_b128 v203, v[10:13] offset:63376
	ds_write_b32 v203, v154 offset:63908
	s_waitcnt lgkmcnt(8)
	v_mfma_f32_32x32x16_f16 v[30:45], v[58:61], v[22:25], v[30:45]
	s_and_saveexec_b64 s[12:13], s[6:7]
	s_andn2_b64 s[10:11], s[34:35], exec
	s_and_b64 s[38:39], s[8:9], exec
	s_or_b64 s[10:11], s[10:11], s[38:39]
	ds_write_b32 v203, v154 offset:63896
	s_or_b64 exec, exec, s[12:13]
	s_and_saveexec_b64 s[12:13], s[10:11]
	ds_write_b32 v203, v154 offset:63920
	s_or_b64 exec, exec, s[12:13]
	s_movk_i32 s10, 0x420
	v_mad_u32_u24 v10, v54, s10, 0
	s_waitcnt lgkmcnt(5)
	v_mfma_f32_32x32x16_f16 v[30:45], v[70:73], v[50:53], v[30:45]
	v_add_u32_e32 v209, v10, v55
	s_waitcnt lgkmcnt(4)
	v_mfma_f32_32x32x16_f16 v[30:45], v[62:65], v[26:29], v[30:45]
	s_and_saveexec_b64 s[10:11], s[2:3]
	s_cbranch_execz .LBB8_50
	s_mov_b64 s[38:39], s[34:35]
	ds_write_b128 v209, v[6:9] offset:63376
	ds_write_b32 v209, v155 offset:63908
	s_and_saveexec_b64 s[12:13], s[6:7]
	s_andn2_b64 s[38:39], s[34:35], exec
	s_and_b64 s[40:41], s[8:9], exec
	s_or_b64 s[38:39], s[38:39], s[40:41]
	ds_write_b32 v209, v155 offset:63896
	s_or_b64 exec, exec, s[12:13]
	s_and_b64 exec, exec, s[38:39]
	ds_write_b32 v209, v155 offset:63920

.LBB8_55:
	s_or_b64 exec, exec, s[10:11]
	v_mov_b32_e32 v159, 0
	v_mov_b32_e32 v161, 0
	v_mov_b32_e32 v14, 0
	v_mov_b32_e32 v15, 0
	v_mov_b32_e32 v16, 0
	v_mov_b32_e32 v17, 0
	s_and_saveexec_b64 s[10:11], s[26:27]
	s_cbranch_execz .LBB8_57
	v_or_b32_e32 v2, 0x220, v166
	v_ashrrev_i32_e32 v3, 31, v2
	v_lshl_add_u64 v[2:3], v[2:3], 4, s[16:17]
	global_load_dwordx4 v[14:17], v[2:3], off
	v_lshl_add_u64 v[2:3], v[166:167], 2, s[18:19]
	global_load_dword v161, v[2:3], off offset:2176

.LBB8_63:
	s_or_b64 exec, exec, s[10:11]
	s_waitcnt lgkmcnt(0)
	s_barrier
	ds_read_b128 v[18:21], v204 offset:63360
	ds_read_b128 v[22:25], v205 offset:63360
	v_add_u32_e32 v211, 0xf780, v204
	v_add_u32_e32 v212, 0xf780, v205
	s_waitcnt lgkmcnt(1)
	v_mfma_f32_32x32x16_f16 v[42:57], v[150:153], v[18:21], 0
	ds_read_b128 v[18:21], v204 offset:64416
	ds_read_b128 v[26:29], v204 offset:65472
	ds_read_b128 v[154:157], v205 offset:64416
	ds_read_b128 v[162:165], v205 offset:65472
	s_waitcnt lgkmcnt(4)
	v_mfma_f32_32x32x16_f16 v[42:57], v[146:149], v[22:25], v[42:57]
	s_waitcnt lgkmcnt(3)
	v_mfma_f32_32x32x16_f16 v[42:57], v[142:145], v[18:21], v[42:57]
	ds_read_b128 v[18:21], v211 offset:3168
	ds_read_b128 v[22:25], v212 offset:3168
	s_waitcnt lgkmcnt(3)
	v_mfma_f32_32x32x16_f16 v[42:57], v[134:137], v[154:157], v[42:57]
	v_mfma_f32_32x32x16_f16 v[42:57], v[138:141], v[26:29], v[42:57]
	ds_read_b128 v[26:29], v211 offset:4224
	ds_read_b128 v[154:157], v212 offset:4224
	s_waitcnt lgkmcnt(4)
	v_mfma_f32_32x32x16_f16 v[42:57], v[130:133], v[162:165], v[42:57]
	s_waitcnt lgkmcnt(3)
	v_mfma_f32_32x32x16_f16 v[42:57], v[126:129], v[18:21], v[42:57]
	ds_read_b128 v[18:21], v211 offset:5280
	ds_read_b128 v[162:165], v212 offset:5280
	s_waitcnt lgkmcnt(4)
	v_mfma_f32_32x32x16_f16 v[42:57], v[118:121], v[22:25], v[42:57]
	s_waitcnt lgkmcnt(3)
	v_mfma_f32_32x32x16_f16 v[42:57], v[122:125], v[26:29], v[42:57]
	ds_read_b128 v[22:25], v211 offset:10560
	ds_read_b128 v[184:187], v212 offset:10560
	s_waitcnt lgkmcnt(4)
	v_mfma_f32_32x32x16_f16 v[42:57], v[110:113], v[154:157], v[42:57]
	s_waitcnt lgkmcnt(3)
	v_mfma_f32_32x32x16_f16 v[42:57], v[114:117], v[18:21], v[42:57]
	ds_read_b128 v[18:21], v211 offset:11616
	ds_read_b128 v[214:217], v212 offset:11616
	s_waitcnt lgkmcnt(4)
	v_mfma_f32_32x32x16_f16 v[42:57], v[102:105], v[162:165], v[42:57]
	s_waitcnt lgkmcnt(3)
	v_mfma_f32_32x32x16_f16 v[42:57], v[106:109], v[22:25], v[42:57]
	ds_read_b128 v[26:29], v211 offset:12672
	ds_read_b128 v[154:157], v212 offset:12672
	s_waitcnt lgkmcnt(4)
	v_mfma_f32_32x32x16_f16 v[42:57], v[98:101], v[184:187], v[42:57]
	s_waitcnt lgkmcnt(3)
	v_mfma_f32_32x32x16_f16 v[42:57], v[94:97], v[18:21], v[42:57]
	ds_read_b128 v[22:25], v211 offset:13728
	ds_read_b128 v[18:21], v212 offset:13728
	s_mov_b64 s[10:11], s[34:35]
	s_waitcnt vmcnt(1)
	ds_write_b128 v202, v[14:17] offset:16
	s_waitcnt vmcnt(0)
	ds_write_b32 v202, v161 offset:548
	s_waitcnt lgkmcnt(6)
	v_mfma_f32_32x32x16_f16 v[42:57], v[86:89], v[214:217], v[42:57]
	s_and_saveexec_b64 s[12:13], s[6:7]
	s_andn2_b64 s[10:11], s[34:35], exec
	s_and_b64 s[38:39], s[8:9], exec
	s_or_b64 s[10:11], s[10:11], s[38:39]
	ds_write_b32 v202, v161 offset:536
	s_or_b64 exec, exec, s[12:13]
	s_and_saveexec_b64 s[12:13], s[10:11]
	ds_write_b32 v202, v161 offset:560
	s_or_b64 exec, exec, s[12:13]
	v_lshlrev_b32_e32 v14, 11, v198
	s_add_i32 s38, 0, 0x1ef00
	v_lshlrev_b32_e32 v15, 2, v197
	v_cmp_eq_u32_e64 s[10:11], 0, v199
	v_cmp_ne_u32_e64 s[12:13], 0, v199
	v_add3_u32 v206, s38, v14, v15
	s_waitcnt lgkmcnt(5)
	v_mfma_f32_32x32x16_f16 v[42:57], v[90:93], v[26:29], v[42:57]
	ds_read_b128 v[26:29], v211 offset:14784
	ds_read_b128 v[14:17], v212 offset:14784
	s_waitcnt lgkmcnt(6)
	v_mfma_f32_32x32x16_f16 v[42:57], v[82:85], v[154:157], v[42:57]
	s_and_saveexec_b64 s[38:39], s[12:13]
	s_xor_b64 s[38:39], exec, s[38:39]
	v_add_f32_e32 v38, 0, v38
	v_add_f32_e32 v39, 0, v39
	ds_write2st64_b32 v206, v38, v39 offset1:1
	s_andn2_saveexec_b64 s[38:39], s[38:39]
	s_or_b64 exec, exec, s[38:39]
	s_and_saveexec_b64 s[38:39], s[12:13]
	s_xor_b64 s[38:39], exec, s[38:39]
	v_add_f32_e32 v38, 0, v40
	v_add_f32_e32 v39, 0, v41
	ds_write2st64_b32 v206, v38, v39 offset0:2 offset1:3
	s_andn2_saveexec_b64 s[38:39], s[38:39]
	s_or_b64 exec, exec, s[38:39]
	s_waitcnt lgkmcnt(5)
	v_mfma_f32_32x32x16_f16 v[42:57], v[78:81], v[22:25], v[42:57]
	ds_read_b128 v[38:41], v211 offset:15840
	ds_read_b128 v[22:25], v212 offset:15840
	s_mov_b64 s[38:39], s[34:35]
	ds_write_b128 v203, v[10:13] offset:16
	ds_write_b32 v203, v159 offset:548
	s_waitcnt lgkmcnt(8)
	v_mfma_f32_32x32x16_f16 v[42:57], v[58:61], v[18:21], v[42:57]
	s_and_saveexec_b64 s[40:41], s[6:7]
	s_andn2_b64 s[38:39], s[34:35], exec
	s_and_b64 s[42:43], s[8:9], exec
	s_or_b64 s[38:39], s[38:39], s[42:43]
	ds_write_b32 v203, v159 offset:536
	s_or_b64 exec, exec, s[40:41]
	s_and_saveexec_b64 s[40:41], s[38:39]
	ds_write_b32 v203, v159 offset:560
	s_or_b64 exec, exec, s[40:41]
	s_waitcnt lgkmcnt(5)
	v_mfma_f32_32x32x16_f16 v[42:57], v[70:73], v[26:29], v[42:57]
	s_waitcnt lgkmcnt(4)
	v_mfma_f32_32x32x16_f16 v[42:57], v[62:65], v[14:17], v[42:57]
	s_and_saveexec_b64 s[38:39], s[2:3]
	s_cbranch_execz .LBB8_80
	s_mov_b64 s[42:43], s[34:35]
	ds_write_b128 v209, v[6:9] offset:16
	ds_write_b32 v209, v160 offset:548
	s_and_saveexec_b64 s[40:41], s[6:7]
	s_andn2_b64 s[42:43], s[34:35], exec
	s_and_b64 s[44:45], s[8:9], exec
	s_or_b64 s[42:43], s[42:43], s[44:45]
	ds_write_b32 v209, v160 offset:536
	s_or_b64 exec, exec, s[40:41]
	s_and_b64 exec, exec, s[42:43]
	ds_write_b32 v209, v160 offset:560

.LBB8_85:
	s_or_b64 exec, exec, s[38:39]
	v_mov_b32_e32 v175, 0
	v_mov_b32_e32 v185, 0
	v_mov_b32_e32 v38, 0
	v_mov_b32_e32 v39, 0
	v_mov_b32_e32 v40, 0
	v_mov_b32_e32 v41, 0
	s_and_saveexec_b64 s[38:39], s[26:27]
	s_cbranch_execz .LBB8_87
	v_or_b32_e32 v2, 0x240, v166
	v_ashrrev_i32_e32 v3, 31, v2
	v_lshl_add_u64 v[2:3], v[2:3], 4, s[16:17]
	global_load_dwordx4 v[38:41], v[2:3], off
	v_lshl_add_u64 v[2:3], v[166:167], 2, s[18:19]
	global_load_dword v185, v[2:3], off offset:2304

.LBB8_93:
	s_or_b64 exec, exec, s[38:39]
	s_waitcnt lgkmcnt(0)
	s_barrier
	ds_read_b128 v[2:5], v204
	ds_read_b128 v[54:57], v205
	ds_read_b128 v[154:157], v204 offset:1056
	ds_read_b128 v[158:161], v204 offset:2112
	ds_read_b128 v[162:165], v205 offset:1056
	ds_read_b128 v[186:189], v205 offset:2112
	s_waitcnt lgkmcnt(5)
	v_mfma_f32_32x32x16_f16 v[2:17], v[150:153], v[2:5], 0
	s_waitcnt lgkmcnt(4)
	v_mfma_f32_32x32x16_f16 v[2:17], v[146:149], v[54:57], v[2:17]
	s_waitcnt lgkmcnt(3)
	v_mfma_f32_32x32x16_f16 v[2:17], v[142:145], v[154:157], v[2:17]
	ds_read_b128 v[54:57], v204 offset:3168
	ds_read_b128 v[154:157], v205 offset:3168
	s_waitcnt lgkmcnt(3)
	v_mfma_f32_32x32x16_f16 v[2:17], v[134:137], v[162:165], v[2:17]
	v_mfma_f32_32x32x16_f16 v[2:17], v[138:141], v[158:161], v[2:17]
	ds_read_b128 v[158:161], v204 offset:4224
	ds_read_b128 v[162:165], v205 offset:4224
	s_waitcnt lgkmcnt(4)
	v_mfma_f32_32x32x16_f16 v[2:17], v[130:133], v[186:189], v[2:17]
	s_waitcnt lgkmcnt(3)
	v_mfma_f32_32x32x16_f16 v[2:17], v[126:129], v[54:57], v[2:17]
	ds_read_b128 v[54:57], v204 offset:5280
	ds_read_b128 v[186:189], v205 offset:5280
	s_waitcnt lgkmcnt(4)
	v_mfma_f32_32x32x16_f16 v[2:17], v[118:121], v[154:157], v[2:17]
	s_waitcnt lgkmcnt(3)
	v_mfma_f32_32x32x16_f16 v[2:17], v[122:125], v[158:161], v[2:17]
	ds_read_b128 v[154:157], v204 offset:10560
	ds_read_b128 v[214:217], v205 offset:10560
	s_waitcnt lgkmcnt(4)
	v_mfma_f32_32x32x16_f16 v[2:17], v[110:113], v[162:165], v[2:17]
	s_waitcnt lgkmcnt(3)
	v_mfma_f32_32x32x16_f16 v[2:17], v[114:117], v[54:57], v[2:17]
	ds_read_b128 v[54:57], v204 offset:11616
	ds_read_b128 v[218:221], v205 offset:11616
	s_waitcnt lgkmcnt(4)
	v_mfma_f32_32x32x16_f16 v[2:17], v[102:105], v[186:189], v[2:17]
	s_waitcnt lgkmcnt(3)
	v_mfma_f32_32x32x16_f16 v[2:17], v[106:109], v[154:157], v[2:17]
	ds_read_b128 v[158:161], v204 offset:12672
	ds_read_b128 v[162:165], v205 offset:12672
	s_waitcnt lgkmcnt(4)
	v_mfma_f32_32x32x16_f16 v[2:17], v[98:101], v[214:217], v[2:17]
	s_waitcnt lgkmcnt(3)
	v_mfma_f32_32x32x16_f16 v[2:17], v[94:97], v[54:57], v[2:17]
	ds_read_b128 v[154:157], v204 offset:13728
	ds_read_b128 v[54:57], v205 offset:13728
	s_mov_b64 s[38:39], s[34:35]
	s_waitcnt vmcnt(1)
	ds_write_b128 v202, v[38:41] offset:63376
	s_waitcnt vmcnt(0)
	ds_write_b32 v202, v185 offset:63908
	s_waitcnt lgkmcnt(6)
	v_mfma_f32_32x32x16_f16 v[2:17], v[86:89], v[218:221], v[2:17]
	s_and_saveexec_b64 s[40:41], s[6:7]
	s_andn2_b64 s[38:39], s[34:35], exec
	s_and_b64 s[42:43], s[8:9], exec
	s_or_b64 s[38:39], s[38:39], s[42:43]
	ds_write_b32 v202, v185 offset:63896
	s_or_b64 exec, exec, s[40:41]
	s_and_saveexec_b64 s[40:41], s[38:39]
	ds_write_b32 v202, v185 offset:63920
	s_or_b64 exec, exec, s[40:41]
	s_waitcnt lgkmcnt(5)
	v_mfma_f32_32x32x16_f16 v[2:17], v[90:93], v[158:161], v[2:17]
	ds_read_b128 v[158:161], v204 offset:14784
	ds_read_b128 v[38:41], v205 offset:14784
	s_waitcnt lgkmcnt(6)
	v_mfma_f32_32x32x16_f16 v[2:17], v[82:85], v[162:165], v[2:17]
	s_and_saveexec_b64 s[38:39], s[12:13]
	s_xor_b64 s[38:39], exec, s[38:39]
	v_add_f32_e32 v35, 0, v35
	v_add_f32_e32 v34, 0, v34
	v_add_f32_e32 v34, v34, v50
	v_add_f32_e32 v35, v35, v51
	ds_write2st64_b32 v206, v34, v35 offset0:4 offset1:5
	s_andn2_saveexec_b64 s[38:39], s[38:39]
	s_or_b64 exec, exec, s[38:39]
	s_and_saveexec_b64 s[38:39], s[12:13]
	s_xor_b64 s[38:39], exec, s[38:39]
	v_add_f32_e32 v34, 0, v37
	v_add_f32_e32 v35, 0, v36
	v_add_f32_e32 v35, v35, v52
	v_add_f32_e32 v34, v34, v53
	ds_write2st64_b32 v206, v35, v34 offset0:6 offset1:7
	s_andn2_saveexec_b64 s[38:39], s[38:39]
	s_or_b64 exec, exec, s[38:39]
	s_waitcnt lgkmcnt(5)
	v_mfma_f32_32x32x16_f16 v[2:17], v[78:81], v[154:157], v[2:17]
	ds_read_b128 v[50:53], v204 offset:15840
	ds_read_b128 v[34:37], v205 offset:15840
	s_mov_b64 s[38:39], s[34:35]
	ds_write_b128 v203, v[26:29] offset:63376
	ds_write_b32 v203, v175 offset:63908
	s_waitcnt lgkmcnt(8)
	v_mfma_f32_32x32x16_f16 v[2:17], v[58:61], v[54:57], v[2:17]
	s_and_saveexec_b64 s[40:41], s[6:7]
	s_andn2_b64 s[38:39], s[34:35], exec
	s_and_b64 s[42:43], s[8:9], exec
	s_or_b64 s[38:39], s[38:39], s[42:43]
	ds_write_b32 v203, v175 offset:63896
	s_or_b64 exec, exec, s[40:41]
	s_and_saveexec_b64 s[40:41], s[38:39]
	ds_write_b32 v203, v175 offset:63920
	s_or_b64 exec, exec, s[40:41]
	s_waitcnt lgkmcnt(5)
	v_mfma_f32_32x32x16_f16 v[2:17], v[70:73], v[158:161], v[2:17]
	s_waitcnt lgkmcnt(4)
	v_mfma_f32_32x32x16_f16 v[2:17], v[62:65], v[38:41], v[2:17]
	s_and_saveexec_b64 s[38:39], s[2:3]
	s_cbranch_execz .LBB8_110
	s_mov_b64 s[42:43], s[34:35]
	ds_write_b128 v209, v[22:25] offset:63376
	ds_write_b32 v209, v184 offset:63908
	s_and_saveexec_b64 s[40:41], s[6:7]
	s_andn2_b64 s[42:43], s[34:35], exec
	s_and_b64 s[44:45], s[8:9], exec
	s_or_b64 s[42:43], s[42:43], s[44:45]
	ds_write_b32 v209, v184 offset:63896
	s_or_b64 exec, exec, s[40:41]
	s_and_b64 exec, exec, s[42:43]
	ds_write_b32 v209, v184 offset:63920

.LBB8_115:
	s_or_b64 exec, exec, s[38:39]
	v_mov_b32_e32 v175, 0
	v_mov_b32_e32 v185, 0
	v_mov_b32_e32 v54, 0
	v_mov_b32_e32 v55, 0
	v_mov_b32_e32 v56, 0
	v_mov_b32_e32 v57, 0
	s_and_saveexec_b64 s[38:39], s[26:27]
	s_cbranch_execz .LBB8_117
	v_or_b32_e32 v14, 0x260, v166
	v_ashrrev_i32_e32 v15, 31, v14
	v_lshl_add_u64 v[14:15], v[14:15], 4, s[16:17]
	global_load_dwordx4 v[54:57], v[14:15], off
	v_lshl_add_u64 v[14:15], v[166:167], 2, s[18:19]
	global_load_dword v185, v[14:15], off offset:2432

.LBB8_123:
	s_or_b64 exec, exec, s[14:15]
	s_waitcnt lgkmcnt(0)
	s_barrier
	ds_read_b128 v[14:17], v204 offset:63360
	ds_read_b128 v[154:157], v205 offset:63360
	ds_read_b128 v[158:161], v204 offset:64416
	ds_read_b128 v[162:165], v204 offset:65472
	ds_read_b128 v[166:169], v205 offset:64416
	ds_read_b128 v[170:173], v205 offset:65472
	s_waitcnt lgkmcnt(5)
	v_mfma_f32_32x32x16_f16 v[14:29], v[150:153], v[14:17], 0
	s_waitcnt lgkmcnt(4)
	v_mfma_f32_32x32x16_f16 v[14:29], v[146:149], v[154:157], v[14:29]
	s_waitcnt lgkmcnt(3)
	v_mfma_f32_32x32x16_f16 v[14:29], v[142:145], v[158:161], v[14:29]
	ds_read_b128 v[154:157], v211 offset:3168
	ds_read_b128 v[158:161], v212 offset:3168
	s_waitcnt lgkmcnt(3)
	v_mfma_f32_32x32x16_f16 v[14:29], v[134:137], v[166:169], v[14:29]
	v_mfma_f32_32x32x16_f16 v[14:29], v[138:141], v[162:165], v[14:29]
	ds_read_b128 v[162:165], v211 offset:4224
	ds_read_b128 v[166:169], v212 offset:4224
	s_waitcnt lgkmcnt(4)
	v_mfma_f32_32x32x16_f16 v[14:29], v[130:133], v[170:173], v[14:29]
	s_waitcnt lgkmcnt(3)
	v_mfma_f32_32x32x16_f16 v[14:29], v[126:129], v[154:157], v[14:29]
	ds_read_b128 v[154:157], v211 offset:5280
	ds_read_b128 v[170:173], v212 offset:5280
	s_waitcnt lgkmcnt(4)
	v_mfma_f32_32x32x16_f16 v[14:29], v[118:121], v[158:161], v[14:29]
	s_waitcnt lgkmcnt(3)
	v_mfma_f32_32x32x16_f16 v[14:29], v[122:125], v[162:165], v[14:29]
	ds_read_b128 v[158:161], v211 offset:10560
	ds_read_b128 v[186:189], v212 offset:10560
	s_waitcnt lgkmcnt(4)
	v_mfma_f32_32x32x16_f16 v[14:29], v[110:113], v[166:169], v[14:29]
	s_waitcnt lgkmcnt(3)
	v_mfma_f32_32x32x16_f16 v[14:29], v[114:117], v[154:157], v[14:29]
	ds_read_b128 v[154:157], v211 offset:11616
	ds_read_b128 v[214:217], v212 offset:11616
	s_waitcnt lgkmcnt(4)
	v_mfma_f32_32x32x16_f16 v[14:29], v[102:105], v[170:173], v[14:29]
	s_waitcnt lgkmcnt(3)
	v_mfma_f32_32x32x16_f16 v[14:29], v[106:109], v[158:161], v[14:29]
	ds_read_b128 v[162:165], v211 offset:12672
	ds_read_b128 v[166:169], v212 offset:12672
	s_waitcnt lgkmcnt(4)
	v_mfma_f32_32x32x16_f16 v[14:29], v[98:101], v[186:189], v[14:29]
	s_waitcnt lgkmcnt(3)
	v_mfma_f32_32x32x16_f16 v[14:29], v[94:97], v[154:157], v[14:29]
	ds_read_b128 v[158:161], v211 offset:13728
	ds_read_b128 v[154:157], v212 offset:13728
	s_mov_b64 s[14:15], s[34:35]
	s_waitcnt vmcnt(1)
	ds_write_b128 v202, v[54:57] offset:16
	s_waitcnt vmcnt(0)
	ds_write_b32 v202, v185 offset:548
	s_waitcnt lgkmcnt(6)
	v_mfma_f32_32x32x16_f16 v[14:29], v[86:89], v[214:217], v[14:29]
	s_and_saveexec_b64 s[36:37], s[6:7]
	s_andn2_b64 s[14:15], s[34:35], exec
	s_and_b64 s[38:39], s[8:9], exec
	s_or_b64 s[14:15], s[14:15], s[38:39]
	ds_write_b32 v202, v185 offset:536
	s_or_b64 exec, exec, s[36:37]
	s_and_saveexec_b64 s[36:37], s[14:15]
	ds_write_b32 v202, v185 offset:560
	s_or_b64 exec, exec, s[36:37]
	v_add_f32_e32 v31, v31, v47
	v_add_f32_e32 v46, v30, v46
	s_waitcnt lgkmcnt(5)
	v_mfma_f32_32x32x16_f16 v[14:29], v[90:93], v[162:165], v[14:29]
	ds_read_b128 v[162:165], v211 offset:14784
	ds_read_b128 v[54:57], v212 offset:14784
	v_mov_b32_e32 v170, v10
	v_mov_b32_e32 v171, v42
	v_mov_b32_e32 v47, v6
	v_pk_add_f32 v[170:171], v[170:171], v[46:47]
	v_add_f32_e32 v221, v31, v11
	s_waitcnt lgkmcnt(6)
	v_mfma_f32_32x32x16_f16 v[14:29], v[82:85], v[166:169], v[14:29]
	s_and_saveexec_b64 s[14:15], s[12:13]
	s_xor_b64 s[14:15], exec, s[14:15]
	v_add_f32_e32 v221, v31, v11
	ds_write2st64_b32 v206, v170, v221 offset1:1
	s_andn2_saveexec_b64 s[14:15], s[14:15]
	s_or_b64 exec, exec, s[14:15]
	v_add_f32_e32 v6, v33, v49
	v_add_f32_e32 v10, v32, v48
	v_add_f32_e32 v223, v10, v12
	v_add_f32_e32 v222, v6, v13
	s_and_saveexec_b64 s[14:15], s[12:13]
	s_xor_b64 s[14:15], exec, s[14:15]
	v_add_f32_e32 v222, v6, v13
	ds_write2st64_b32 v206, v223, v222 offset0:2 offset1:3
	s_andn2_saveexec_b64 s[14:15], s[14:15]
	s_or_b64 exec, exec, s[14:15]
	s_waitcnt lgkmcnt(5)
	v_mfma_f32_32x32x16_f16 v[14:29], v[78:81], v[158:161], v[14:29]
	ds_read_b128 v[30:33], v211 offset:15840
	ds_read_b128 v[10:13], v212 offset:15840
	s_mov_b64 s[14:15], s[34:35]
	ds_write_b128 v203, v[50:53] offset:16
	ds_write_b32 v203, v175 offset:548
	s_waitcnt lgkmcnt(8)
	v_mfma_f32_32x32x16_f16 v[14:29], v[58:61], v[154:157], v[14:29]
	s_and_saveexec_b64 s[36:37], s[6:7]
	s_andn2_b64 s[14:15], s[34:35], exec
	s_and_b64 s[38:39], s[8:9], exec
	s_or_b64 s[14:15], s[14:15], s[38:39]
	ds_write_b32 v203, v175 offset:536
	s_or_b64 exec, exec, s[36:37]
	s_and_saveexec_b64 s[36:37], s[14:15]
	ds_write_b32 v203, v175 offset:560
	s_or_b64 exec, exec, s[36:37]
	s_waitcnt lgkmcnt(5)
	v_mfma_f32_32x32x16_f16 v[14:29], v[70:73], v[162:165], v[14:29]
	s_waitcnt lgkmcnt(4)
	v_mfma_f32_32x32x16_f16 v[14:29], v[62:65], v[54:57], v[14:29]
	s_and_saveexec_b64 s[14:15], s[2:3]
	s_cbranch_execz .LBB8_140
	s_mov_b64 s[38:39], s[34:35]
	ds_write_b128 v209, v[38:41] offset:16
	ds_write_b32 v209, v184 offset:548
	s_and_saveexec_b64 s[36:37], s[6:7]
	s_andn2_b64 s[38:39], s[34:35], exec
	s_and_b64 s[40:41], s[8:9], exec
	s_or_b64 s[38:39], s[38:39], s[40:41]
	ds_write_b32 v209, v184 offset:536
	s_or_b64 exec, exec, s[36:37]
	s_and_b64 exec, exec, s[38:39]
	ds_write_b32 v209, v184 offset:560

.LBB8_269:
	s_or_b64 exec, exec, s[10:11]
	v_mov_b32_e32 v152, 0
	v_mov_b32_e32 v44, 0
	v_mov_b32_e32 v12, 0
	v_mov_b32_e32 v13, 0
	v_mov_b32_e32 v14, 0
	v_mov_b32_e32 v15, 0
	s_and_saveexec_b64 s[10:11], s[26:27]
	s_cbranch_execz .LBB8_271
	s_lshl_b32 s12, s53, 10
	v_or3_b32 v0, v1, s12, v192
	v_lshl_or_b32 v0, v0, 10, v190
	v_ashrrev_i32_e32 v1, 31, v0
	v_lshl_add_u64 v[2:3], v[0:1], 4, s[16:17]
	v_lshl_add_u64 v[0:1], v[0:1], 2, s[18:19]
	global_load_dwordx4 v[12:15], v[2:3], off offset:512
	global_load_dword v44, v[0:1], off offset:128

.LBB8_277:
	s_or_b64 exec, exec, s[10:11]
	v_and_b32_e32 v185, 2, v198
	v_lshlrev_b32_e32 v17, 2, v198
	v_lshl_add_u32 v16, v199, 1, v185
	v_and_b32_e32 v186, 4, v17
	v_mad_u32_u24 v16, v16, 10, v186
	v_mul_u32_u24_e32 v24, 0x420, v16
	v_add_lshl_u32 v16, v191, v190, 4
	v_add3_u32 v187, v24, v16, 0
	s_waitcnt lgkmcnt(0)
	s_barrier
	ds_read_b128 v[16:19], v187 offset:63360
	v_mov_b32_e32 v20, 0x220
	v_cmp_gt_u32_e64 s[10:11], 32, v197
	v_add_u32_e32 v188, 0xf780, v187
	s_nop 0
	v_cndmask_b32_e64 v20, v20, 32, s[10:11]
	v_add_u32_e32 v25, v20, v167
	ds_read_b128 v[20:23], v187 offset:64416
	s_waitcnt vmcnt(23) lgkmcnt(1)
	v_mfma_f32_32x32x16_f16 v[28:43], v[52:55], v[16:19], 0
	v_add3_u32 v189, v25, v24, 0
	ds_read_b128 v[16:19], v189 offset:63360
	ds_read_b128 v[24:27], v187 offset:65472
	ds_read_b128 v[46:49], v189 offset:64416
	ds_read_b128 v[154:157], v189 offset:65472
	v_add_u32_e32 v200, 0xf780, v189
	s_waitcnt vmcnt(22) lgkmcnt(3)
	v_mfma_f32_32x32x16_f16 v[28:43], v[56:59], v[16:19], v[28:43]
	s_waitcnt vmcnt(21)
	v_mfma_f32_32x32x16_f16 v[28:43], v[60:63], v[20:23], v[28:43]
	ds_read_b128 v[16:19], v188 offset:3168
	ds_read_b128 v[20:23], v200 offset:3168
	s_waitcnt vmcnt(20) lgkmcnt(3)
	v_mfma_f32_32x32x16_f16 v[28:43], v[64:67], v[46:49], v[28:43]
	s_waitcnt vmcnt(19)
	v_mfma_f32_32x32x16_f16 v[28:43], v[68:71], v[24:27], v[28:43]
	ds_read_b128 v[24:27], v188 offset:4224
	ds_read_b128 v[46:49], v200 offset:4224
	s_waitcnt vmcnt(18) lgkmcnt(4)
	v_mfma_f32_32x32x16_f16 v[28:43], v[72:75], v[154:157], v[28:43]
	s_waitcnt vmcnt(17) lgkmcnt(3)
	v_mfma_f32_32x32x16_f16 v[28:43], v[76:79], v[16:19], v[28:43]
	ds_read_b128 v[16:19], v188 offset:5280
	ds_read_b128 v[154:157], v200 offset:5280
	s_waitcnt vmcnt(16) lgkmcnt(4)
	v_mfma_f32_32x32x16_f16 v[28:43], v[80:83], v[20:23], v[28:43]
	s_waitcnt vmcnt(15) lgkmcnt(3)
	v_mfma_f32_32x32x16_f16 v[28:43], v[84:87], v[24:27], v[28:43]
	ds_read_b128 v[20:23], v188 offset:10560
	ds_read_b128 v[158:161], v200 offset:10560
	s_waitcnt vmcnt(14) lgkmcnt(4)
	v_mfma_f32_32x32x16_f16 v[28:43], v[88:91], v[46:49], v[28:43]
	s_waitcnt vmcnt(13) lgkmcnt(3)
	v_mfma_f32_32x32x16_f16 v[28:43], v[92:95], v[16:19], v[28:43]
	ds_read_b128 v[16:19], v188 offset:11616
	ds_read_b128 v[176:179], v200 offset:11616
	s_waitcnt vmcnt(12) lgkmcnt(4)
	v_mfma_f32_32x32x16_f16 v[28:43], v[96:99], v[154:157], v[28:43]
	s_waitcnt vmcnt(11) lgkmcnt(3)
	v_mfma_f32_32x32x16_f16 v[28:43], v[100:103], v[20:23], v[28:43]
	ds_read_b128 v[24:27], v188 offset:12672
	ds_read_b128 v[48:51], v200 offset:12672
	s_waitcnt vmcnt(10) lgkmcnt(4)
	v_mfma_f32_32x32x16_f16 v[28:43], v[104:107], v[158:161], v[28:43]
	s_waitcnt vmcnt(9) lgkmcnt(3)
	v_mfma_f32_32x32x16_f16 v[28:43], v[108:111], v[16:19], v[28:43]
	ds_read_b128 v[16:19], v188 offset:13728
	ds_read_b128 v[20:23], v200 offset:13728
	s_mov_b64 s[10:11], s[20:21]
	s_waitcnt vmcnt(1)
	ds_write_b128 v183, v[12:15] offset:16
	s_waitcnt vmcnt(0)
	ds_write_b32 v183, v44 offset:548
	s_waitcnt lgkmcnt(6)
	v_mfma_f32_32x32x16_f16 v[28:43], v[112:115], v[176:179], v[28:43]
	s_and_saveexec_b64 s[12:13], s[6:7]
	s_andn2_b64 s[10:11], s[20:21], exec
	s_and_b64 s[22:23], s[8:9], exec
	s_or_b64 s[10:11], s[10:11], s[22:23]
	ds_write_b32 v183, v44 offset:536
	s_or_b64 exec, exec, s[12:13]
	s_and_saveexec_b64 s[12:13], s[10:11]
	ds_write_b32 v183, v44 offset:560
	s_or_b64 exec, exec, s[12:13]
	s_waitcnt lgkmcnt(5)
	v_mfma_f32_32x32x16_f16 v[28:43], v[116:119], v[24:27], v[28:43]
	ds_read_b128 v[44:47], v188 offset:14784
	ds_read_b128 v[24:27], v200 offset:14784
	v_cmp_eq_u32_e64 s[10:11], 0, v199
	v_cmp_ne_u32_e64 s[12:13], 0, v199
	v_lshlrev_b32_e32 v169, 11, v198
	v_lshlrev_b32_e32 v176, 2, v197
	s_waitcnt lgkmcnt(6)
	v_mfma_f32_32x32x16_f16 v[28:43], v[120:123], v[48:51], v[28:43]
	s_and_saveexec_b64 s[22:23], s[12:13]
	s_cbranch_execz .LBB8_283
	s_add_i32 s36, 0, 0x1ef00
	v_add3_u32 v12, s36, v169, v176
	v_mov_b32_e32 v13, 0
	ds_write2st64_b32 v12, v13, v13 offset1:1
	ds_write2st64_b32 v12, v13, v13 offset0:2 offset1:3

.LBB8_297:
	s_or_b64 exec, exec, s[22:23]
	s_lshl_b32 s47, s53, 10
	v_add_lshl_u32 v0, s47, v192, 10
	v_lshl_add_u32 v0, v196, 15, v0
	v_or_b32_e32 v156, v0, v190
	v_mov_b32_e32 v178, 0
	v_ashrrev_i32_e32 v157, 31, v156
	v_mov_b32_e32 v196, 0
	s_nop 1
	v_mov_b32_e32 v40, 0
	v_mov_b32_e32 v41, 0
	v_mov_b32_e32 v42, 0
	v_mov_b32_e32 v43, 0
	s_and_saveexec_b64 s[22:23], s[26:27]
	s_cbranch_execz .LBB8_299
	v_lshl_add_u64 v[0:1], v[156:157], 4, s[16:17]
	global_load_dwordx4 v[40:43], v[0:1], off offset:1024
	v_lshl_add_u64 v[0:1], v[156:157], 2, s[18:19]
	global_load_dword v196, v[0:1], off offset:256

.LBB8_305:
	s_or_b64 exec, exec, s[22:23]
	s_waitcnt lgkmcnt(0)
	s_barrier
	ds_read_b128 v[0:3], v187
	ds_read_b128 v[44:47], v189
	ds_read_b128 v[48:51], v187 offset:1056
	ds_read_b128 v[148:151], v187 offset:2112
	ds_read_b128 v[152:155], v189 offset:1056
	ds_read_b128 v[202:205], v189 offset:2112
	s_waitcnt lgkmcnt(5)
	v_mfma_f32_32x32x16_f16 v[0:15], v[52:55], v[0:3], 0
	s_waitcnt lgkmcnt(4)
	v_mfma_f32_32x32x16_f16 v[0:15], v[56:59], v[44:47], v[0:15]
	s_waitcnt lgkmcnt(3)
	v_mfma_f32_32x32x16_f16 v[0:15], v[60:63], v[48:51], v[0:15]
	ds_read_b128 v[44:47], v187 offset:3168
	ds_read_b128 v[48:51], v189 offset:3168
	s_waitcnt lgkmcnt(3)
	v_mfma_f32_32x32x16_f16 v[0:15], v[64:67], v[152:155], v[0:15]
	v_mfma_f32_32x32x16_f16 v[0:15], v[68:71], v[148:151], v[0:15]
	ds_read_b128 v[148:151], v187 offset:4224
	ds_read_b128 v[152:155], v189 offset:4224
	s_waitcnt lgkmcnt(4)
	v_mfma_f32_32x32x16_f16 v[0:15], v[72:75], v[202:205], v[0:15]
	s_waitcnt lgkmcnt(3)
	v_mfma_f32_32x32x16_f16 v[0:15], v[76:79], v[44:47], v[0:15]
	ds_read_b128 v[44:47], v187 offset:5280
	ds_read_b128 v[202:205], v189 offset:5280
	s_waitcnt lgkmcnt(4)
	v_mfma_f32_32x32x16_f16 v[0:15], v[80:83], v[48:51], v[0:15]
	s_waitcnt lgkmcnt(3)
	v_mfma_f32_32x32x16_f16 v[0:15], v[84:87], v[148:151], v[0:15]
	ds_read_b128 v[48:51], v187 offset:10560
	ds_read_b128 v[206:209], v189 offset:10560
	s_waitcnt lgkmcnt(4)
	v_mfma_f32_32x32x16_f16 v[0:15], v[88:91], v[152:155], v[0:15]
	s_waitcnt lgkmcnt(3)
	v_mfma_f32_32x32x16_f16 v[0:15], v[92:95], v[44:47], v[0:15]
	ds_read_b128 v[44:47], v187 offset:11616
	ds_read_b128 v[210:213], v189 offset:11616
	s_waitcnt lgkmcnt(4)
	v_mfma_f32_32x32x16_f16 v[0:15], v[96:99], v[202:205], v[0:15]
	s_waitcnt lgkmcnt(3)
	v_mfma_f32_32x32x16_f16 v[0:15], v[100:103], v[48:51], v[0:15]
	ds_read_b128 v[148:151], v187 offset:12672
	ds_read_b128 v[152:155], v189 offset:12672
	s_waitcnt lgkmcnt(4)
	v_mfma_f32_32x32x16_f16 v[0:15], v[104:107], v[206:209], v[0:15]
	s_waitcnt lgkmcnt(3)
	v_mfma_f32_32x32x16_f16 v[0:15], v[108:111], v[44:47], v[0:15]
	ds_read_b128 v[48:51], v187 offset:13728
	ds_read_b128 v[44:47], v189 offset:13728
	s_mov_b64 s[22:23], s[20:21]
	s_waitcnt vmcnt(1)
	ds_write_b128 v183, v[40:43] offset:63376
	s_waitcnt vmcnt(0)
	ds_write_b32 v183, v196 offset:63908
	s_waitcnt lgkmcnt(6)
	v_mfma_f32_32x32x16_f16 v[0:15], v[112:115], v[210:213], v[0:15]
	s_and_saveexec_b64 s[36:37], s[6:7]
	s_andn2_b64 s[22:23], s[20:21], exec
	s_and_b64 s[38:39], s[8:9], exec
	s_or_b64 s[22:23], s[22:23], s[38:39]
	ds_write_b32 v183, v196 offset:63896
	s_or_b64 exec, exec, s[36:37]
	s_and_saveexec_b64 s[36:37], s[22:23]
	ds_write_b32 v183, v196 offset:63920
	s_or_b64 exec, exec, s[36:37]
	s_add_i32 s22, 0, 0x1ef00
	v_add3_u32 v196, s22, v169, v176
	s_waitcnt lgkmcnt(5)
	v_mfma_f32_32x32x16_f16 v[0:15], v[116:119], v[148:151], v[0:15]
	ds_read_b128 v[148:151], v187 offset:14784
	ds_read_b128 v[40:43], v189 offset:14784
	s_waitcnt lgkmcnt(6)
	v_mfma_f32_32x32x16_f16 v[0:15], v[120:123], v[152:155], v[0:15]
	s_and_saveexec_b64 s[22:23], s[12:13]
	s_xor_b64 s[22:23], exec, s[22:23]
	v_add_f32_e32 v36, 0, v36
	v_add_f32_e32 v37, 0, v37
	ds_write2st64_b32 v196, v36, v37 offset0:4 offset1:5
	s_andn2_saveexec_b64 s[22:23], s[22:23]
	s_or_b64 exec, exec, s[22:23]
	s_and_saveexec_b64 s[22:23], s[12:13]
	s_xor_b64 s[22:23], exec, s[22:23]
	v_add_f32_e32 v36, 0, v38
	v_add_f32_e32 v37, 0, v39
	ds_write2st64_b32 v196, v36, v37 offset0:6 offset1:7
	s_andn2_saveexec_b64 s[22:23], s[22:23]
	s_or_b64 exec, exec, s[22:23]
	s_waitcnt lgkmcnt(5)
	v_mfma_f32_32x32x16_f16 v[0:15], v[124:127], v[48:51], v[0:15]
	ds_read_b128 v[48:51], v187 offset:15840
	ds_read_b128 v[36:39], v189 offset:15840
	s_mov_b64 s[22:23], s[20:21]
	ds_write_b128 v184, v[24:27] offset:63376
	ds_write_b32 v184, v178 offset:63908
	s_waitcnt lgkmcnt(8)
	v_mfma_f32_32x32x16_f16 v[0:15], v[128:131], v[44:47], v[0:15]
	s_and_saveexec_b64 s[36:37], s[6:7]
	s_andn2_b64 s[22:23], s[20:21], exec
	s_and_b64 s[38:39], s[8:9], exec
	s_or_b64 s[22:23], s[22:23], s[38:39]
	ds_write_b32 v184, v178 offset:63896
	s_or_b64 exec, exec, s[36:37]
	s_and_saveexec_b64 s[36:37], s[22:23]
	ds_write_b32 v184, v178 offset:63920
	s_or_b64 exec, exec, s[36:37]
	s_movk_i32 s22, 0x420
	v_mad_u32_u24 v24, v166, s22, 0
	s_waitcnt lgkmcnt(5)
	v_mfma_f32_32x32x16_f16 v[0:15], v[132:135], v[148:151], v[0:15]
	v_add_u32_e32 v197, v24, v167
	s_waitcnt lgkmcnt(4)
	v_mfma_f32_32x32x16_f16 v[0:15], v[136:139], v[40:43], v[0:15]
	s_and_saveexec_b64 s[22:23], s[2:3]
	s_cbranch_execz .LBB8_322
	s_mov_b64 s[38:39], s[20:21]
	ds_write_b128 v197, v[20:23] offset:63376
	ds_write_b32 v197, v179 offset:63908
	s_and_saveexec_b64 s[36:37], s[6:7]
	s_andn2_b64 s[38:39], s[20:21], exec
	s_and_b64 s[40:41], s[8:9], exec
	s_or_b64 s[38:39], s[38:39], s[40:41]
	ds_write_b32 v197, v179 offset:63896
	s_or_b64 exec, exec, s[36:37]
	s_and_b64 exec, exec, s[38:39]
	ds_write_b32 v197, v179 offset:63920

.LBB8_327:
	s_or_b64 exec, exec, s[22:23]
	v_mov_b32_e32 v167, 0
	v_mov_b32_e32 v168, 0
	v_mov_b32_e32 v48, 0
	v_mov_b32_e32 v49, 0
	v_mov_b32_e32 v50, 0
	v_mov_b32_e32 v51, 0
	s_and_saveexec_b64 s[22:23], s[26:27]
	s_cbranch_execz .LBB8_329
	v_lshl_add_u64 v[12:13], v[156:157], 4, s[16:17]
	global_load_dwordx4 v[48:51], v[12:13], off offset:1536
	v_lshl_add_u64 v[12:13], v[156:157], 2, s[18:19]
	global_load_dword v168, v[12:13], off offset:384

.LBB8_335:
	s_or_b64 exec, exec, s[14:15]
	s_waitcnt lgkmcnt(0)
	s_barrier
	ds_read_b128 v[12:15], v187 offset:63360
	ds_read_b128 v[148:151], v189 offset:63360
	ds_read_b128 v[152:155], v187 offset:64416
	ds_read_b128 v[156:159], v187 offset:65472
	ds_read_b128 v[160:163], v189 offset:64416
	ds_read_b128 v[202:205], v189 offset:65472
	s_waitcnt lgkmcnt(5)
	v_mfma_f32_32x32x16_f16 v[12:27], v[52:55], v[12:15], 0
	s_waitcnt lgkmcnt(4)
	v_mfma_f32_32x32x16_f16 v[12:27], v[56:59], v[148:151], v[12:27]
	s_waitcnt lgkmcnt(3)
	v_mfma_f32_32x32x16_f16 v[12:27], v[60:63], v[152:155], v[12:27]
	ds_read_b128 v[148:151], v188 offset:3168
	ds_read_b128 v[152:155], v200 offset:3168
	s_waitcnt lgkmcnt(3)
	v_mfma_f32_32x32x16_f16 v[12:27], v[64:67], v[160:163], v[12:27]
	v_mfma_f32_32x32x16_f16 v[12:27], v[68:71], v[156:159], v[12:27]
	ds_read_b128 v[156:159], v188 offset:4224
	ds_read_b128 v[160:163], v200 offset:4224
	s_waitcnt lgkmcnt(4)
	v_mfma_f32_32x32x16_f16 v[12:27], v[72:75], v[202:205], v[12:27]
	s_waitcnt lgkmcnt(3)
	v_mfma_f32_32x32x16_f16 v[12:27], v[76:79], v[148:151], v[12:27]
	ds_read_b128 v[148:151], v188 offset:5280
	ds_read_b128 v[202:205], v200 offset:5280
	s_waitcnt lgkmcnt(4)
	v_mfma_f32_32x32x16_f16 v[12:27], v[80:83], v[152:155], v[12:27]
	s_waitcnt lgkmcnt(3)
	v_mfma_f32_32x32x16_f16 v[12:27], v[84:87], v[156:159], v[12:27]
	ds_read_b128 v[152:155], v188 offset:10560
	ds_read_b128 v[206:209], v200 offset:10560
	s_waitcnt lgkmcnt(4)
	v_mfma_f32_32x32x16_f16 v[12:27], v[88:91], v[160:163], v[12:27]
	s_waitcnt lgkmcnt(3)
	v_mfma_f32_32x32x16_f16 v[12:27], v[92:95], v[148:151], v[12:27]
	ds_read_b128 v[148:151], v188 offset:11616
	ds_read_b128 v[210:213], v200 offset:11616
	s_waitcnt lgkmcnt(4)
	v_mfma_f32_32x32x16_f16 v[12:27], v[96:99], v[202:205], v[12:27]
	s_waitcnt lgkmcnt(3)
	v_mfma_f32_32x32x16_f16 v[12:27], v[100:103], v[152:155], v[12:27]
	ds_read_b128 v[156:159], v188 offset:12672
	ds_read_b128 v[160:163], v200 offset:12672
	s_waitcnt lgkmcnt(4)
	v_mfma_f32_32x32x16_f16 v[12:27], v[104:107], v[206:209], v[12:27]
	s_waitcnt lgkmcnt(3)
	v_mfma_f32_32x32x16_f16 v[12:27], v[108:111], v[148:151], v[12:27]
	ds_read_b128 v[152:155], v188 offset:13728
	ds_read_b128 v[148:151], v200 offset:13728
	s_mov_b64 s[14:15], s[20:21]
	s_waitcnt vmcnt(1)
	ds_write_b128 v183, v[48:51] offset:16
	s_waitcnt vmcnt(0)
	ds_write_b32 v183, v168 offset:548
	s_waitcnt lgkmcnt(6)
	v_mfma_f32_32x32x16_f16 v[12:27], v[112:115], v[210:213], v[12:27]
	s_and_saveexec_b64 s[22:23], s[6:7]
	s_andn2_b64 s[14:15], s[20:21], exec
	s_and_b64 s[26:27], s[8:9], exec
	s_or_b64 s[14:15], s[14:15], s[26:27]
	ds_write_b32 v183, v168 offset:536
	s_or_b64 exec, exec, s[22:23]
	s_and_saveexec_b64 s[22:23], s[14:15]
	ds_write_b32 v183, v168 offset:560
	s_or_b64 exec, exec, s[22:23]
	v_add_f32_e32 v33, 0, v33
	v_add_f32_e32 v168, 0, v32
	s_waitcnt lgkmcnt(5)
	v_mfma_f32_32x32x16_f16 v[12:27], v[116:119], v[156:159], v[12:27]
	ds_read_b128 v[156:159], v188 offset:14784
	ds_read_b128 v[48:51], v200 offset:14784
	v_mov_b32_e32 v176, v8
	v_mov_b32_e32 v177, v28
	v_mov_b32_e32 v169, v4
	v_pk_add_f32 v[168:169], v[176:177], v[168:169]
	v_add_f32_e32 v176, v33, v9
	s_waitcnt lgkmcnt(6)
	v_mfma_f32_32x32x16_f16 v[12:27], v[120:123], v[160:163], v[12:27]
	s_and_saveexec_b64 s[14:15], s[12:13]
	s_xor_b64 s[14:15], exec, s[14:15]
	v_add_f32_e32 v176, v33, v9
	ds_write2st64_b32 v196, v168, v176 offset1:1
	s_andn2_saveexec_b64 s[14:15], s[14:15]
	s_or_b64 exec, exec, s[14:15]
	v_add_f32_e32 v4, 0, v35
	v_add_f32_e32 v8, 0, v34
	v_add_f32_e32 v178, v8, v10
	v_add_f32_e32 v177, v4, v11
	s_and_saveexec_b64 s[14:15], s[12:13]
	s_xor_b64 s[14:15], exec, s[14:15]
	v_add_f32_e32 v177, v4, v11
	ds_write2st64_b32 v196, v178, v177 offset0:2 offset1:3
	s_andn2_saveexec_b64 s[14:15], s[14:15]
	s_or_b64 exec, exec, s[14:15]
	s_waitcnt lgkmcnt(5)
	v_mfma_f32_32x32x16_f16 v[12:27], v[124:127], v[152:155], v[12:27]
	ds_read_b128 v[32:35], v188 offset:15840
	ds_read_b128 v[8:11], v200 offset:15840
	s_mov_b64 s[14:15], s[20:21]
	ds_write_b128 v184, v[44:47] offset:16
	ds_write_b32 v184, v167 offset:548
	s_waitcnt lgkmcnt(8)
	v_mfma_f32_32x32x16_f16 v[12:27], v[128:131], v[148:151], v[12:27]
	s_and_saveexec_b64 s[22:23], s[6:7]
	s_andn2_b64 s[14:15], s[20:21], exec
	s_and_b64 s[26:27], s[8:9], exec
	s_or_b64 s[14:15], s[14:15], s[26:27]
	ds_write_b32 v184, v167 offset:536
	s_or_b64 exec, exec, s[22:23]
	s_and_saveexec_b64 s[22:23], s[14:15]
	ds_write_b32 v184, v167 offset:560
	s_or_b64 exec, exec, s[22:23]
	s_waitcnt lgkmcnt(5)
	v_mfma_f32_32x32x16_f16 v[12:27], v[132:135], v[156:159], v[12:27]
	s_waitcnt lgkmcnt(4)
	v_mfma_f32_32x32x16_f16 v[12:27], v[136:139], v[48:51], v[12:27]
	s_and_saveexec_b64 s[14:15], s[2:3]
	s_cbranch_execz .LBB8_352
	s_mov_b64 s[26:27], s[20:21]
	ds_write_b128 v197, v[40:43] offset:16
	ds_write_b32 v197, v179 offset:548
	s_and_saveexec_b64 s[22:23], s[6:7]
	s_andn2_b64 s[26:27], s[20:21], exec
	s_and_b64 s[34:35], s[8:9], exec
	s_or_b64 s[26:27], s[26:27], s[34:35]
	ds_write_b32 v197, v179 offset:536
	s_or_b64 exec, exec, s[22:23]
	s_and_b64 exec, exec, s[26:27]
	ds_write_b32 v197, v179 offset:560
